# cache policy: nt also on the prep phase's wide (dwordx4) output stores
# speedup vs baseline: 1.0112x; 1.0016x over previous
; __device__ __forceinline__ void gla_pass_a(KP Pk, Frame& F, int l, int it, LAS unsigned char* wl) {
;     ...
;         float* sl = cg < GGRP ? (float*)(ws + WS_GSL) + ((size_t)seq * NCH + c) * 2048 : (float*)(ws + WS_GGS) + ((size_t)seq * NGRP + g) * 2048;
;         float* al = cg < GGRP ? (float*)(ws + WS_GAE) + ((size_t)seq * NCH + c) * 32 : (float*)(ws + WS_GGA) + ((size_t)seq * NGRP + g) * 32;
; #pragma unroll
;         for (int db = 0; db < 2; ++db)
; #pragma unroll
;             for (int nb = 0; nb < 4; ++nb)
; #pragma unroll
;                 for (int i = 0; i < 4; ++i) sl[(16 * db + 4 * kg + i) * 64 + 16 * nb + r16] = Sr[db][nb][i];
;         if ((F.lane & 15) == 0) {
; #pragma unroll
;             for (int j = 0; j < 8; ++j) al[kg * 8 + j] = __expf(ltot[j]); }
.LBB0_345:
	s_add_i32 s27, s54, s31
	s_cmp_lg_u32 s54, 6
	s_cselect_b64 s[34:35], -1, 0
	s_ashr_i32 s37, s27, 31
	v_readlane_b32 s40, v253, 50
	s_add_u32 s46, s40, s27
	v_readlane_b32 s27, v253, 49
	s_addc_u32 s47, s27, s37
	s_lshl_b64 s[40:41], s[46:47], 13
	s_add_u32 s27, s4, s40
	s_addc_u32 s37, s5, s41
	s_cmp_eq_u32 s54, 6
	s_cselect_b64 s[48:49], -1, 0
	s_and_b64 s[40:41], s[48:49], exec
	s_cselect_b32 s41, s7, s37
	s_cselect_b32 s40, s6, s27
	v_lshl_add_u64 v[42:43], v[102:103], 2, s[40:41]
	global_store_dword v[42:43], v38, off
	v_lshl_add_u64 v[42:43], v[104:105], 2, s[40:41]
	v_lshl_add_u64 v[44:45], v[114:115], 2, s[40:41]
	global_store_dword v[42:43], v39, off offset:256
	global_store_dword v[42:43], v40, off offset:512
	global_store_dword v[42:43], v41, off offset:768
	global_store_dword v[42:43], v30, off offset:64
	global_store_dword v[44:45], v31, off offset:256
	global_store_dword v[44:45], v32, off offset:512
	global_store_dword v[44:45], v33, off offset:768
	global_store_dword v[42:43], v22, off offset:128
	v_lshl_add_u64 v[44:45], v[116:117], 2, s[40:41]
	global_store_dword v[44:45], v23, off offset:256
	global_store_dword v[44:45], v24, off offset:512
	global_store_dword v[44:45], v25, off offset:768
	global_store_dword v[42:43], v14, off offset:192
	v_lshl_add_u64 v[42:43], v[118:119], 2, s[40:41]
	global_store_dword v[42:43], v15, off offset:256
	global_store_dword v[42:43], v16, off offset:512
	global_store_dword v[42:43], v17, off offset:768
	v_lshl_add_u64 v[42:43], v[106:107], 2, s[40:41]
	global_store_dword v[42:43], v34, off
	v_lshl_add_u64 v[42:43], v[108:109], 2, s[40:41]
	global_store_dword v[42:43], v35, off
	v_lshl_add_u64 v[42:43], v[110:111], 2, s[40:41]
	global_store_dword v[42:43], v36, off
	v_lshl_add_u64 v[42:43], v[112:113], 2, s[40:41]
	global_store_dword v[42:43], v37, off
	v_lshl_add_u64 v[42:43], v[120:121], 2, s[40:41]
	v_lshl_add_u64 v[44:45], v[122:123], 2, s[40:41]
	v_lshl_add_u64 v[46:47], v[124:125], 2, s[40:41]
	v_lshl_add_u64 v[48:49], v[126:127], 2, s[40:41]
	global_store_dword v[42:43], v26, off offset:64
	global_store_dword v[44:45], v27, off offset:64
	global_store_dword v[46:47], v28, off offset:64
	global_store_dword v[48:49], v29, off offset:64
	global_store_dword v[42:43], v18, off offset:128
	global_store_dword v[44:45], v19, off offset:128
	global_store_dword v[46:47], v20, off offset:128
	global_store_dword v[48:49], v21, off offset:128
	global_store_dword v[42:43], v10, off offset:192
	global_store_dword v[44:45], v11, off offset:192
	global_store_dword v[46:47], v12, off offset:192
	global_store_dword v[48:49], v13, off offset:192
	s_and_saveexec_b64 s[40:41], s[38:39]
	s_cbranch_execz .LBB0_347
	s_lshl_b64 s[46:47], s[46:47], 7
	s_add_u32 s27, s18, s46
	s_addc_u32 s37, s19, s47
	s_and_b64 s[46:47], s[48:49], exec
	v_mul_f32_e32 v1, 0x3fb8aa3b, v2
	s_cselect_b32 s37, s51, s37
	s_cselect_b32 s27, s50, s27
	v_exp_f32_e32 v42, v1
	v_mul_f32_e32 v1, 0x3fb8aa3b, v3
	v_mov_b32_e32 v44, s27
	v_mov_b32_e32 v45, s37
	v_exp_f32_e32 v43, v1
	v_mul_f32_e32 v1, 0x3fb8aa3b, v4
	v_lshl_add_u64 v[46:47], v[100:101], 2, v[44:45]
	v_exp_f32_e32 v44, v1
	v_mul_f32_e32 v1, 0x3fb8aa3b, v5
	v_exp_f32_e32 v45, v1
	v_mul_f32_e32 v1, 0x3fb8aa3b, v6
	global_store_dwordx4 v[46:47], v[42:45], off nt
	s_nop 1
	v_exp_f32_e32 v42, v1
	v_mul_f32_e32 v1, 0x3fb8aa3b, v7
	v_exp_f32_e32 v43, v1
	v_mul_f32_e32 v1, 0x3fb8aa3b, v8
	v_exp_f32_e32 v44, v1
	v_mul_f32_e32 v1, 0x3fb8aa3b, v9
	v_exp_f32_e32 v45, v1
	global_store_dwordx4 v[46:47], v[42:45], off offset:16 nt

; __device__ __forceinline__ unsigned pk2(float lo, float hi) { return f2bf(lo) | (f2bf(hi) << 16); }
; __device__ __forceinline__ float dpp_x1(float v) { return __builtin_bit_cast(float, __builtin_amdgcn_update_dpp(0, __builtin_bit_cast(int, v), 0xB1, 0xF, 0xF, true)); }
; __device__ __forceinline__ float dpp_x2(float v) { return __builtin_bit_cast(float, __builtin_amdgcn_update_dpp(0, __builtin_bit_cast(int, v), 0x4E, 0xF, 0xF, true)); }
; __device__ __forceinline__ float dpp_hm(float v) { return __builtin_bit_cast(float, __builtin_amdgcn_update_dpp(0, __builtin_bit_cast(int, v), 0x141, 0xF, 0xF, true)); }
; __device__ __forceinline__ void qk_vec(bf16_t* p, const u32x4 r, const float (&w)[8], const float (&cs)[8], const float (&sn)[8]) {
;     float x[8] = {bflo(r.x), bfhi(r.x), bflo(r.y), bfhi(r.y), bflo(r.z), bfhi(r.z), bflo(r.w), bfhi(r.w)};
;     float ss = 0.f;
; #pragma unroll
;     for (int e = 0; e < 8; ++e) ss += x[e] * x[e];
;     ss += dpp_x1(ss); ss += dpp_x2(ss); ss += dpp_hm(ss);
;     const float rstd = rsqrtf(ss * (1.f / 64.f) + NORM_EPS);
;     float o[8];
; #pragma unroll
;     for (int e = 0; e < 8; ++e) { const float y = x[e] * rstd * w[e]; o[e] = y * cs[e] + dpp_x2(y) * sn[e]; }
;     u32x4 q; q.x = pk2(o[0], o[1]); q.y = pk2(o[2], o[3]); q.z = pk2(o[4], o[5]); q.w = pk2(o[6], o[7]);
;     *(u32x4*)p = q;
; }
; __device__ __forceinline__ void prep_qk_rows4(KP Pk, Frame& F, int l, int row0) {
;     ...
;     { const float* a = Pk->in[I_SQN] + l * 64 + 8 * j; const float* b = Pk->in[I_DQN] + l * 64 + 8 * j; const float* c = Pk->in[I_DKN] + l * 64 + 8 * j; const float* d = Pk->in[I_SKN] + l * 64 + 8 * j;
; #pragma unroll
;       for (int e = 0; e < 8; ++e) { wsq[e] = a[e] * qs; wdq[e] = b[e] * qs; wdk[e] = c[e]; wsk[e] = d[e]; } }
;     float cs[4][8], sn[4][8], csk[8], snk[8];
; #pragma unroll
;     for (int r = 0; r < 4; ++r) qk_rope(ws, row0 + r, j, cs[r], sn[r]);
;     qk_rope(ws, rowk, j, csk, snk);
;     asm volatile("" ::: "memory");
; #pragma unroll
;     for (int r = 0; r < 4; ++r) { bf16_t* up = U + (size_t)(row0 + r) * NU + 8 * F.lane;
;         qk_vec(up + UC_SQ, raw[r][0], wsq, cs[r], sn[r]); qk_vec(up + UC_DQ, raw[r][1], wdq, cs[r], sn[r]); qk_vec(up + UC_DK, raw[r][2], wdk, cs[r], sn[r]); }
.LBB0_385:
	s_or_b64 exec, exec, s[8:9]
	s_mov_b64 s[8:9], 0x1e00
	v_lshl_add_u64 v[224:225], v[198:199], 0, s[8:9]
	v_lshl_add_u64 v[220:221], v[162:163], 0, s[8:9]
	v_lshl_add_u64 v[216:217], v[134:135], 0, s[8:9]
	v_lshl_add_u64 v[178:179], v[132:133], 0, s[8:9]
	s_mov_b64 s[8:9], 0x1000
	v_lshl_add_u64 v[160:161], v[160:161], 0, s[8:9]
	s_mov_b32 s8, 0x3e38aa3b
	s_waitcnt vmcnt(0)
	v_mov_b32_e32 v16, v107
	v_mov_b32_e32 v20, v103
	v_mov_b32_e32 v21, v105
	v_mov_b32_e32 v107, v108
	v_mov_b32_e32 v12, v111
	v_mov_b32_e32 v13, v113
	v_mov_b32_e32 v111, v112
	v_pk_mul_f32 v[112:113], v[20:21], s[8:9] op_sel_hi:[1,0]
	v_pk_mul_f32 v[20:21], v[106:107], s[8:9] op_sel_hi:[1,0]
	v_lshlrev_b32_e32 v106, 16, v98
	v_and_b32_e32 v108, 0xffff0000, v98
	v_mov_b32_e32 v8, v115
	v_mov_b32_e32 v115, v116
	v_mov_b32_e32 v17, v109
	v_lshlrev_b32_e32 v107, 16, v99
	v_and_b32_e32 v109, 0xffff0000, v99
	v_mov_b32_e32 v98, v106
	v_mov_b32_e32 v99, v108
	v_pk_mul_f32 v[196:197], v[12:13], s[8:9] op_sel_hi:[1,0]
	v_pk_mul_f32 v[12:13], v[114:115], s[8:9] op_sel_hi:[1,0]
	v_pk_mul_f32 v[98:99], v[98:99], v[98:99]
	v_mov_b32_e32 v114, v109
	v_mov_b32_e32 v115, v107
	v_pk_mul_f32 v[114:115], v[114:115], v[114:115]
	v_lshlrev_b32_e32 v116, 16, v100
	v_and_b32_e32 v100, 0xffff0000, v100
	v_add_f32_e32 v67, v98, v99
	v_mov_b32_e32 v242, v100
	v_mov_b32_e32 v243, v116
	v_add_f32_e32 v67, v115, v67
	v_mov_b32_e32 v9, v117
	v_lshlrev_b32_e32 v117, 16, v101
	v_and_b32_e32 v101, 0xffff0000, v101
	v_pk_mul_f32 v[242:243], v[242:243], v[242:243]
	v_add_f32_e32 v67, v114, v67
	v_mov_b32_e32 v244, v101
	v_mov_b32_e32 v245, v117
	v_add_f32_e32 v67, v243, v67
	v_pk_mul_f32 v[244:245], v[244:245], v[244:245]
	v_add_f32_e32 v67, v242, v67
	v_add_f32_e32 v67, v245, v67
	v_add_f32_e32 v67, v244, v67
	v_mov_b32_e32 v103, v104
	v_pk_mul_f32 v[98:99], v[102:103], s[8:9] op_sel_hi:[1,0]
	v_add_f32_dpp v67, v67, v67 quad_perm:[1,0,3,2] row_mask:0xf bank_mask:0xf bound_ctrl:1
	v_pk_mul_f32 v[110:111], v[110:111], s[8:9] op_sel_hi:[1,0]
	s_mov_b64 s[18:19], 0x2200
	v_add_f32_dpp v67, v67, v67 quad_perm:[2,3,0,1] row_mask:0xf bank_mask:0xf bound_ctrl:1
	v_lshl_add_u64 v[222:223], v[198:199], 0, s[18:19]
	v_and_b32_e32 v244, 0xffff0000, v92
	v_add_f32_dpp v67, v67, v67 row_half_mirror row_mask:0xf bank_mask:0xf bound_ctrl:1
	v_fmamk_f32 v67, v67, 0x3c800000, v194
	v_mul_f32_e32 v69, 0x4b800000, v67
	v_cmp_gt_f32_e32 vcc, s66, v67
	v_and_b32_e32 v245, 0xffff0000, v93
	v_mov_b32_e32 v250, v245
	v_cndmask_b32_e32 v67, v67, v69, vcc
	v_rsq_f32_e32 v67, v67
	v_pk_mul_f32 v[8:9], v[8:9], s[8:9] op_sel_hi:[1,0]
	v_pk_mul_f32 v[16:17], v[16:17], s[8:9] op_sel_hi:[1,0]
	s_mov_b32 s8, 0x358637bd
	v_mul_f32_e32 v69, 0x45800000, v67
	v_cndmask_b32_e32 v102, v67, v69, vcc
	v_pk_mul_f32 v[104:105], v[102:103], v[106:107] op_sel_hi:[0,1]
	v_pk_mul_f32 v[104:105], v[98:99], v[104:105]
	v_pk_mul_f32 v[108:109], v[102:103], v[108:109] op_sel_hi:[0,1]
	v_pk_mul_f32 v[108:109], v[112:113], v[108:109]
	v_mov_b32_dpp v106, v104 quad_perm:[2,3,0,1] row_mask:0xf bank_mask:0xf bound_ctrl:1
	v_pk_mul_f32 v[242:243], v[214:215], v[104:105]
	v_mov_b32_dpp v107, v105 quad_perm:[2,3,0,1] row_mask:0xf bank_mask:0xf bound_ctrl:1
	v_mov_b32_dpp v114, v108 quad_perm:[2,3,0,1] row_mask:0xf bank_mask:0xf bound_ctrl:1
	v_pk_fma_f32 v[104:105], v[206:207], v[106:107], v[242:243]
	v_pk_mul_f32 v[106:107], v[212:213], v[108:109]
	v_mov_b32_dpp v115, v109 quad_perm:[2,3,0,1] row_mask:0xf bank_mask:0xf bound_ctrl:1
	v_pk_mul_f32 v[108:109], v[102:103], v[116:117] op_sel_hi:[0,1]
	v_pk_mul_f32 v[108:109], v[110:111], v[108:109]
	v_pk_mul_f32 v[100:101], v[102:103], v[100:101] op_sel_hi:[0,1]
	v_pk_fma_f32 v[106:107], v[202:203], v[114:115], v[106:107]
	v_mov_b32_dpp v114, v108 quad_perm:[2,3,0,1] row_mask:0xf bank_mask:0xf bound_ctrl:1
	v_pk_mul_f32 v[100:101], v[196:197], v[100:101]
	v_pk_mul_f32 v[116:117], v[210:211], v[108:109]
	v_mov_b32_dpp v115, v109 quad_perm:[2,3,0,1] row_mask:0xf bank_mask:0xf bound_ctrl:1
	v_mov_b32_dpp v102, v100 quad_perm:[2,3,0,1] row_mask:0xf bank_mask:0xf bound_ctrl:1
	v_pk_fma_f32 v[108:109], v[200:201], v[114:115], v[116:117]
	v_pk_mul_f32 v[114:115], v[208:209], v[100:101]
	v_mov_b32_dpp v103, v101 quad_perm:[2,3,0,1] row_mask:0xf bank_mask:0xf bound_ctrl:1
	v_pk_fma_f32 v[100:101], v[204:205], v[102:103], v[114:115]
	v_bfe_u32 v83, v104, 16, 1
	v_bfe_u32 v67, v101, 16, 1
	v_bfe_u32 v69, v100, 16, 1
	v_add3_u32 v69, v100, v69, s23
	v_add3_u32 v67, v101, v67, s23
	v_bfe_u32 v100, v105, 16, 1
	v_bfe_u32 v101, v108, 16, 1
	v_bfe_u32 v102, v109, 16, 1
	v_bfe_u32 v71, v107, 16, 1
	v_bfe_u32 v79, v106, 16, 1
	v_add3_u32 v102, v109, v102, s23
	v_add3_u32 v101, v108, v101, s23
	v_add3_u32 v100, v105, v100, s23
	v_add3_u32 v83, v104, v83, s23
	v_add3_u32 v79, v106, v79, s23
	v_add3_u32 v71, v107, v71, s23
	v_lshrrev_b32_e32 v83, 16, v83
	v_lshrrev_b32_e32 v100, 16, v100
	v_lshrrev_b32_e32 v101, 16, v101
	v_lshrrev_b32_e32 v102, 16, v102
	v_and_or_b32 v103, v67, s95, v102
	v_and_or_b32 v102, v69, s95, v101
	v_and_or_b32 v101, v71, s95, v100
	v_and_or_b32 v100, v79, s95, v83
	global_store_dwordx4 v[198:199], v[100:103], off offset:3072 nt
	v_lshlrev_b32_e32 v116, 16, v90
	v_and_b32_e32 v198, 0xffff0000, v90
	v_lshlrev_b32_e32 v100, 16, v94
	v_and_b32_e32 v94, 0xffff0000, v94
	v_mov_b32_e32 v102, v100
	v_mov_b32_e32 v103, v94
	v_lshlrev_b32_e32 v117, 16, v91
	v_and_b32_e32 v199, 0xffff0000, v91
	v_mov_b32_e32 v90, v116
	v_mov_b32_e32 v91, v198
	v_pk_mul_f32 v[102:103], v[102:103], v[102:103]
	v_pk_mul_f32 v[90:91], v[90:91], v[90:91]
	v_lshlrev_b32_e32 v101, 16, v95
	v_and_b32_e32 v95, 0xffff0000, v95
; __device__ __forceinline__ unsigned pk2(float lo, float hi) { return f2bf(lo) | (f2bf(hi) << 16); }
; __device__ __forceinline__ float dpp_x1(float v) { return __builtin_bit_cast(float, __builtin_amdgcn_update_dpp(0, __builtin_bit_cast(int, v), 0xB1, 0xF, 0xF, true)); }
; __device__ __forceinline__ float dpp_x2(float v) { return __builtin_bit_cast(float, __builtin_amdgcn_update_dpp(0, __builtin_bit_cast(int, v), 0x4E, 0xF, 0xF, true)); }
; __device__ __forceinline__ float dpp_hm(float v) { return __builtin_bit_cast(float, __builtin_amdgcn_update_dpp(0, __builtin_bit_cast(int, v), 0x141, 0xF, 0xF, true)); }
; __device__ __forceinline__ void qk_vec(bf16_t* p, const u32x4 r, const float (&w)[8], const float (&cs)[8], const float (&sn)[8]) {
;     float x[8] = {bflo(r.x), bfhi(r.x), bflo(r.y), bfhi(r.y), bflo(r.z), bfhi(r.z), bflo(r.w), bfhi(r.w)};
;     float ss = 0.f;
; #pragma unroll
;     for (int e = 0; e < 8; ++e) ss += x[e] * x[e];
;     ss += dpp_x1(ss); ss += dpp_x2(ss); ss += dpp_hm(ss);
;     const float rstd = rsqrtf(ss * (1.f / 64.f) + NORM_EPS);
;     float o[8];
; #pragma unroll
;     for (int e = 0; e < 8; ++e) { const float y = x[e] * rstd * w[e]; o[e] = y * cs[e] + dpp_x2(y) * sn[e]; }
;     u32x4 q; q.x = pk2(o[0], o[1]); q.y = pk2(o[2], o[3]); q.z = pk2(o[4], o[5]); q.w = pk2(o[6], o[7]);
;     *(u32x4*)p = q;
; }
	v_mov_b32_e32 v242, v90
	v_mov_b32_e32 v243, v102
	v_mov_b32_e32 v102, v91
	v_mov_b32_e32 v104, v95
	v_mov_b32_e32 v105, v101
	v_pk_add_f32 v[90:91], v[242:243], v[102:103]
	v_mov_b32_e32 v102, v199
	v_mov_b32_e32 v103, v117
	v_pk_mul_f32 v[228:229], v[104:105], v[104:105]
	v_lshlrev_b32_e32 v106, 16, v96
	v_and_b32_e32 v96, 0xffff0000, v96
	v_pk_mul_f32 v[102:103], v[102:103], v[102:103]
	v_lshlrev_b32_e32 v242, 16, v92
	v_mov_b32_e32 v108, v96
	v_mov_b32_e32 v109, v106
	v_lshlrev_b32_e32 v243, 16, v93
	v_mov_b32_e32 v92, v244
	v_mov_b32_e32 v93, v242
	v_mov_b32_e32 v104, v103
	v_mov_b32_e32 v105, v229
	v_lshlrev_b32_e32 v107, 16, v97
	v_and_b32_e32 v97, 0xffff0000, v97
	v_pk_mul_f32 v[108:109], v[108:109], v[108:109]
	v_pk_mul_f32 v[92:93], v[92:93], v[92:93]
	v_pk_add_f32 v[90:91], v[104:105], v[90:91]
	v_mov_b32_e32 v103, v228
	v_mov_b32_e32 v114, v97
	v_mov_b32_e32 v115, v107
	v_mov_b32_e32 v251, v243
	v_pk_add_f32 v[90:91], v[102:103], v[90:91]
	v_mov_b32_e32 v102, v93
	v_mov_b32_e32 v103, v109
	v_pk_mul_f32 v[114:115], v[114:115], v[114:115]
	v_pk_mul_f32 v[250:251], v[250:251], v[250:251]
	v_pk_add_f32 v[90:91], v[102:103], v[90:91]
	v_mov_b32_e32 v93, v108
	v_pk_add_f32 v[90:91], v[92:93], v[90:91]
	v_mov_b32_e32 v92, v251
	v_mov_b32_e32 v93, v115
	v_pk_add_f32 v[90:91], v[92:93], v[90:91]
	v_mov_b32_e32 v251, v114
	v_pk_add_f32 v[90:91], v[250:251], v[90:91]
	v_mov_b32_e32 v189, v85
	v_mov_b32_e32 v191, v81
	v_mov_b32_dpp v93, v91 quad_perm:[1,0,3,2] row_mask:0xf bank_mask:0xf bound_ctrl:1
	v_mov_b32_dpp v92, v90 quad_perm:[1,0,3,2] row_mask:0xf bank_mask:0xf bound_ctrl:1
	v_pk_add_f32 v[90:91], v[90:91], v[92:93]
	v_mov_b32_e32 v177, v73
	v_lshl_add_u64 v[218:219], v[162:163], 0, s[18:19]
	v_mov_b32_dpp v93, v91 quad_perm:[2,3,0,1] row_mask:0xf bank_mask:0xf bound_ctrl:1
	v_mov_b32_dpp v92, v90 quad_perm:[2,3,0,1] row_mask:0xf bank_mask:0xf bound_ctrl:1
	v_pk_add_f32 v[90:91], v[90:91], v[92:93]
	v_lshl_add_u64 v[192:193], v[134:135], 0, s[18:19]
	v_lshl_add_u64 v[164:165], v[132:133], 0, s[18:19]
	v_mov_b32_dpp v93, v91 row_half_mirror row_mask:0xf bank_mask:0xf bound_ctrl:1
	v_mov_b32_dpp v92, v90 row_half_mirror row_mask:0xf bank_mask:0xf bound_ctrl:1
	v_pk_add_f32 v[90:91], v[90:91], v[92:93]
	v_mov_b64_e32 v[92:93], s[8:9]
	s_mov_b32 s8, 0x3c800000
	v_pk_fma_f32 v[102:103], v[90:91], s[8:9], v[92:93] op_sel_hi:[1,0,0]
	v_mov_b32_e32 v90, v34
	v_mul_f32_e32 v67, 0x4b800000, v103
	v_cmp_gt_f32_e32 vcc, s66, v103
	v_mov_b32_e32 v91, v36
	v_mov_b32_e32 v36, v35
	v_cndmask_b32_e32 v67, v103, v67, vcc
	v_rsq_f32_e32 v67, v67
	s_nop 0
	v_mul_f32_e32 v34, 0x45800000, v67
	v_cndmask_b32_e32 v34, v67, v34, vcc
	v_pk_mul_f32 v[100:101], v[34:35], v[100:101] op_sel_hi:[0,1]
	v_pk_mul_f32 v[100:101], v[20:21], v[100:101]
	v_pk_mul_f32 v[94:95], v[34:35], v[94:95] op_sel_hi:[0,1]
	v_pk_mul_f32 v[94:95], v[16:17], v[94:95]
	v_mov_b32_dpp v104, v100 quad_perm:[2,3,0,1] row_mask:0xf bank_mask:0xf bound_ctrl:1
	v_pk_mul_f32 v[114:115], v[214:215], v[100:101]
	v_mov_b32_dpp v105, v101 quad_perm:[2,3,0,1] row_mask:0xf bank_mask:0xf bound_ctrl:1
	v_mov_b32_dpp v108, v94 quad_perm:[2,3,0,1] row_mask:0xf bank_mask:0xf bound_ctrl:1
	v_pk_fma_f32 v[100:101], v[206:207], v[104:105], v[114:115]
	v_pk_mul_f32 v[104:105], v[212:213], v[94:95]
	v_mov_b32_dpp v109, v95 quad_perm:[2,3,0,1] row_mask:0xf bank_mask:0xf bound_ctrl:1
	v_pk_fma_f32 v[94:95], v[202:203], v[108:109], v[104:105]
	v_pk_mul_f32 v[104:105], v[34:35], v[106:107] op_sel_hi:[0,1]
	v_pk_mul_f32 v[104:105], v[12:13], v[104:105]
	v_pk_mul_f32 v[34:35], v[34:35], v[96:97] op_sel_hi:[0,1]
	v_pk_mul_f32 v[34:35], v[8:9], v[34:35]
	v_mov_b32_dpp v106, v104 quad_perm:[2,3,0,1] row_mask:0xf bank_mask:0xf bound_ctrl:1
	v_pk_mul_f32 v[108:109], v[210:211], v[104:105]
	v_mov_b32_dpp v107, v105 quad_perm:[2,3,0,1] row_mask:0xf bank_mask:0xf bound_ctrl:1
	v_mov_b32_dpp v96, v34 quad_perm:[2,3,0,1] row_mask:0xf bank_mask:0xf bound_ctrl:1
	v_pk_fma_f32 v[104:105], v[200:201], v[106:107], v[108:109]
	v_pk_mul_f32 v[106:107], v[208:209], v[34:35]
	v_mov_b32_dpp v97, v35 quad_perm:[2,3,0,1] row_mask:0xf bank_mask:0xf bound_ctrl:1
	v_pk_fma_f32 v[34:35], v[204:205], v[96:97], v[106:107]
	v_bfe_u32 v83, v104, 16, 1
	v_bfe_u32 v69, v34, 16, 1
	v_add3_u32 v83, v104, v83, s23
	v_add3_u32 v34, v34, v69, s23
	v_lshrrev_b32_e32 v83, 16, v83
	v_and_or_b32 v96, v34, s95, v83
	v_mul_f32_e32 v34, 0x4b800000, v102
	v_cmp_gt_f32_e32 vcc, s66, v102
	v_bfe_u32 v67, v35, 16, 1
	v_bfe_u32 v79, v94, 16, 1
	v_cndmask_b32_e32 v34, v102, v34, vcc
	v_rsq_f32_e32 v34, v34
	v_add3_u32 v79, v94, v79, s23
	v_add3_u32 v35, v35, v67, s23
	v_bfe_u32 v67, v100, 16, 1
	v_bfe_u32 v69, v101, 16, 1
	v_bfe_u32 v94, v105, 16, 1
	v_bfe_u32 v71, v95, 16, 1
	v_add3_u32 v94, v105, v94, s23
	v_add3_u32 v69, v101, v69, s23
	v_add3_u32 v67, v100, v67, s23
	v_add3_u32 v71, v95, v71, s23
	v_lshrrev_b32_e32 v67, 16, v67
	v_lshrrev_b32_e32 v69, 16, v69
	v_lshrrev_b32_e32 v94, 16, v94
	v_and_or_b32 v97, v35, s95, v94
	v_and_or_b32 v95, v71, s95, v69
	v_and_or_b32 v94, v79, s95, v67
	v_mul_f32_e32 v35, 0x45800000, v34
	global_store_dwordx4 v[224:225], v[94:97], off nt
	v_and_b32_e32 v108, 0xffff0000, v74
	v_and_b32_e32 v109, 0xffff0000, v75
	v_cndmask_b32_e32 v94, v34, v35, vcc
	v_pk_mul_f32 v[34:35], v[94:95], v[116:117] op_sel_hi:[0,1]
	v_pk_mul_f32 v[100:101], v[94:95], v[198:199] op_sel_hi:[0,1]
	v_pk_mul_f32 v[34:35], v[90:91], v[34:35]
	v_pk_mul_f32 v[100:101], v[36:37], v[100:101]
	v_pk_mul_f32 v[104:105], v[214:215], v[34:35]
	v_mov_b32_dpp v96, v34 quad_perm:[2,3,0,1] row_mask:0xf bank_mask:0xf bound_ctrl:1
; __device__ __forceinline__ unsigned pk2(float lo, float hi) { return f2bf(lo) | (f2bf(hi) << 16); }
; __device__ __forceinline__ float dpp_x1(float v) { return __builtin_bit_cast(float, __builtin_amdgcn_update_dpp(0, __builtin_bit_cast(int, v), 0xB1, 0xF, 0xF, true)); }
; __device__ __forceinline__ float dpp_x2(float v) { return __builtin_bit_cast(float, __builtin_amdgcn_update_dpp(0, __builtin_bit_cast(int, v), 0x4E, 0xF, 0xF, true)); }
; __device__ __forceinline__ float dpp_hm(float v) { return __builtin_bit_cast(float, __builtin_amdgcn_update_dpp(0, __builtin_bit_cast(int, v), 0x141, 0xF, 0xF, true)); }
; __device__ __forceinline__ void qk_vec(bf16_t* p, const u32x4 r, const float (&w)[8], const float (&cs)[8], const float (&sn)[8]) {
;     float x[8] = {bflo(r.x), bfhi(r.x), bflo(r.y), bfhi(r.y), bflo(r.z), bfhi(r.z), bflo(r.w), bfhi(r.w)};
;     float ss = 0.f;
; #pragma unroll
;     for (int e = 0; e < 8; ++e) ss += x[e] * x[e];
;     ss += dpp_x1(ss); ss += dpp_x2(ss); ss += dpp_hm(ss);
;     const float rstd = rsqrtf(ss * (1.f / 64.f) + NORM_EPS);
;     float o[8];
; #pragma unroll
;     for (int e = 0; e < 8; ++e) { const float y = x[e] * rstd * w[e]; o[e] = y * cs[e] + dpp_x2(y) * sn[e]; }
;     u32x4 q; q.x = pk2(o[0], o[1]); q.y = pk2(o[2], o[3]); q.z = pk2(o[4], o[5]); q.w = pk2(o[6], o[7]);
;     *(u32x4*)p = q;
; }
	v_mov_b32_dpp v102, v100 quad_perm:[2,3,0,1] row_mask:0xf bank_mask:0xf bound_ctrl:1
	v_mov_b32_dpp v97, v35 quad_perm:[2,3,0,1] row_mask:0xf bank_mask:0xf bound_ctrl:1
	v_pk_mul_f32 v[34:35], v[212:213], v[100:101]
	v_mov_b32_dpp v103, v101 quad_perm:[2,3,0,1] row_mask:0xf bank_mask:0xf bound_ctrl:1
	v_pk_fma_f32 v[100:101], v[202:203], v[102:103], v[34:35]
	v_pk_mul_f32 v[102:103], v[94:95], v[242:243] op_sel_hi:[0,1]
	v_mov_b32_e32 v34, v26
	v_mov_b32_e32 v35, v28
	v_pk_mul_f32 v[94:95], v[94:95], v[244:245] op_sel_hi:[0,1]
	v_mov_b32_e32 v28, v27
	v_pk_mul_f32 v[102:103], v[34:35], v[102:103]
	v_pk_mul_f32 v[94:95], v[28:29], v[94:95]
	v_pk_fma_f32 v[96:97], v[206:207], v[96:97], v[104:105]
	v_mov_b32_dpp v26, v102 quad_perm:[2,3,0,1] row_mask:0xf bank_mask:0xf bound_ctrl:1
	v_mov_b32_dpp v104, v94 quad_perm:[2,3,0,1] row_mask:0xf bank_mask:0xf bound_ctrl:1
	v_pk_mul_f32 v[106:107], v[210:211], v[102:103]
	v_mov_b32_dpp v27, v103 quad_perm:[2,3,0,1] row_mask:0xf bank_mask:0xf bound_ctrl:1
	v_pk_mul_f32 v[102:103], v[208:209], v[94:95]
	v_mov_b32_dpp v105, v95 quad_perm:[2,3,0,1] row_mask:0xf bank_mask:0xf bound_ctrl:1
	v_pk_fma_f32 v[94:95], v[204:205], v[104:105], v[102:103]
	v_pk_fma_f32 v[26:27], v[200:201], v[26:27], v[106:107]
	v_bfe_u32 v67, v95, 16, 1
	v_bfe_u32 v69, v94, 16, 1
	v_bfe_u32 v79, v100, 16, 1
	v_add3_u32 v79, v100, v79, s23
	v_add3_u32 v69, v94, v69, s23
	v_add3_u32 v67, v95, v67, s23
	v_bfe_u32 v83, v96, 16, 1
	v_bfe_u32 v94, v97, 16, 1
	v_bfe_u32 v95, v26, 16, 1
	v_bfe_u32 v100, v27, 16, 1
	v_bfe_u32 v71, v101, 16, 1
	v_add3_u32 v27, v27, v100, s23
	v_add3_u32 v26, v26, v95, s23
	v_add3_u32 v94, v97, v94, s23
	v_add3_u32 v83, v96, v83, s23
	v_add3_u32 v71, v101, v71, s23
	v_lshrrev_b32_e32 v83, 16, v83
	v_lshrrev_b32_e32 v94, 16, v94
	v_lshrrev_b32_e32 v26, 16, v26
	v_lshrrev_b32_e32 v27, 16, v27
	v_and_or_b32 v97, v67, s95, v27
	v_and_or_b32 v96, v69, s95, v26
	v_and_or_b32 v95, v71, s95, v94
	v_and_or_b32 v94, v79, s95, v83
	v_lshlrev_b32_e32 v26, 16, v86
	v_and_b32_e32 v86, 0xffff0000, v86
	v_lshlrev_b32_e32 v106, 16, v74
	global_store_dwordx4 v[222:223], v[94:97], off nt
	v_lshlrev_b32_e32 v107, 16, v75
	v_mov_b32_e32 v74, v106
	v_mov_b32_e32 v94, v26
	v_mov_b32_e32 v95, v86
	v_mov_b32_e32 v75, v108
	v_pk_mul_f32 v[94:95], v[94:95], v[94:95]
	v_pk_mul_f32 v[74:75], v[74:75], v[74:75]
	v_lshlrev_b32_e32 v27, 16, v87
	v_and_b32_e32 v87, 0xffff0000, v87
	v_mov_b32_e32 v114, v74
	v_mov_b32_e32 v115, v94
	v_mov_b32_e32 v94, v75
	v_mov_b32_e32 v96, v87
	v_mov_b32_e32 v97, v27
	v_pk_add_f32 v[74:75], v[114:115], v[94:95]
	v_mov_b32_e32 v94, v109
	v_mov_b32_e32 v95, v107
	v_pk_mul_f32 v[96:97], v[96:97], v[96:97]
	v_lshlrev_b32_e32 v100, 16, v88
	v_and_b32_e32 v88, 0xffff0000, v88
	v_pk_mul_f32 v[94:95], v[94:95], v[94:95]
	v_lshlrev_b32_e32 v114, 16, v76
	v_and_b32_e32 v116, 0xffff0000, v76
	v_mov_b32_e32 v102, v88
	v_mov_b32_e32 v103, v100
	v_lshlrev_b32_e32 v115, 16, v77
	v_and_b32_e32 v117, 0xffff0000, v77
	v_mov_b32_e32 v76, v116
	v_mov_b32_e32 v77, v114
	v_mov_b32_e32 v200, v95
	v_mov_b32_e32 v201, v97
	v_lshlrev_b32_e32 v101, 16, v89
	v_and_b32_e32 v89, 0xffff0000, v89
	v_pk_mul_f32 v[102:103], v[102:103], v[102:103]
	v_pk_mul_f32 v[76:77], v[76:77], v[76:77]
	v_pk_add_f32 v[74:75], v[200:201], v[74:75]
	v_mov_b32_e32 v95, v96
	v_mov_b32_e32 v104, v89
	v_mov_b32_e32 v105, v101
	v_mov_b32_e32 v198, v117
	v_mov_b32_e32 v199, v115
	v_pk_add_f32 v[74:75], v[94:95], v[74:75]
	v_mov_b32_e32 v94, v77
	v_mov_b32_e32 v95, v103
	v_pk_mul_f32 v[104:105], v[104:105], v[104:105]
	v_pk_mul_f32 v[198:199], v[198:199], v[198:199]
	v_pk_add_f32 v[74:75], v[94:95], v[74:75]
	v_mov_b32_e32 v77, v102
	v_pk_add_f32 v[74:75], v[76:77], v[74:75]
	v_mov_b32_e32 v76, v199
	v_mov_b32_e32 v77, v105
	v_pk_add_f32 v[74:75], v[76:77], v[74:75]
	v_mov_b32_e32 v199, v104
	v_pk_add_f32 v[74:75], v[198:199], v[74:75]
	v_mov_b32_e32 v83, v84
	v_mov_b32_e32 v79, v80
	v_mov_b32_dpp v77, v75 quad_perm:[1,0,3,2] row_mask:0xf bank_mask:0xf bound_ctrl:1
	v_mov_b32_dpp v76, v74 quad_perm:[1,0,3,2] row_mask:0xf bank_mask:0xf bound_ctrl:1
	v_pk_add_f32 v[74:75], v[74:75], v[76:77]
	v_lshlrev_b32_e32 v96, 16, v58
	v_lshlrev_b32_e32 v97, 16, v59
	v_mov_b32_dpp v77, v75 quad_perm:[2,3,0,1] row_mask:0xf bank_mask:0xf bound_ctrl:1
	v_mov_b32_dpp v76, v74 quad_perm:[2,3,0,1] row_mask:0xf bank_mask:0xf bound_ctrl:1
	v_pk_add_f32 v[74:75], v[74:75], v[76:77]
	v_and_b32_e32 v104, 0xffff0000, v60
	v_and_b32_e32 v105, 0xffff0000, v61
	v_mov_b32_dpp v77, v75 row_half_mirror row_mask:0xf bank_mask:0xf bound_ctrl:1
	v_mov_b32_dpp v76, v74 row_half_mirror row_mask:0xf bank_mask:0xf bound_ctrl:1
	v_pk_add_f32 v[74:75], v[74:75], v[76:77]
	s_nop 0
	v_pk_fma_f32 v[74:75], v[74:75], s[8:9], v[92:93] op_sel_hi:[1,0,0]
	s_nop 0
	v_mul_f32_e32 v67, 0x4b800000, v75
	v_cmp_gt_f32_e32 vcc, s66, v75
	s_nop 1
	v_cndmask_b32_e32 v67, v75, v67, vcc
	v_rsq_f32_e32 v67, v67
	s_nop 0
	v_mul_f32_e32 v69, 0x45800000, v67
	v_cndmask_b32_e32 v76, v67, v69, vcc
	v_pk_mul_f32 v[26:27], v[76:77], v[26:27] op_sel_hi:[0,1]
	v_pk_mul_f32 v[26:27], v[98:99], v[26:27]
	v_pk_mul_f32 v[84:85], v[76:77], v[86:87] op_sel_hi:[0,1]
	v_pk_mul_f32 v[84:85], v[112:113], v[84:85]
	v_mov_b32_dpp v80, v26 quad_perm:[2,3,0,1] row_mask:0xf bank_mask:0xf bound_ctrl:1
	v_pk_mul_f32 v[94:95], v[82:83], v[26:27]
	v_mov_b32_dpp v81, v27 quad_perm:[2,3,0,1] row_mask:0xf bank_mask:0xf bound_ctrl:1
	v_mov_b32_dpp v86, v84 quad_perm:[2,3,0,1] row_mask:0xf bank_mask:0xf bound_ctrl:1
	v_pk_fma_f32 v[26:27], v[184:185], v[80:81], v[94:95]
	v_pk_mul_f32 v[80:81], v[188:189], v[84:85]
; __device__ __forceinline__ unsigned pk2(float lo, float hi) { return f2bf(lo) | (f2bf(hi) << 16); }
; __device__ __forceinline__ float dpp_x1(float v) { return __builtin_bit_cast(float, __builtin_amdgcn_update_dpp(0, __builtin_bit_cast(int, v), 0xB1, 0xF, 0xF, true)); }
; __device__ __forceinline__ float dpp_x2(float v) { return __builtin_bit_cast(float, __builtin_amdgcn_update_dpp(0, __builtin_bit_cast(int, v), 0x4E, 0xF, 0xF, true)); }
; __device__ __forceinline__ float dpp_hm(float v) { return __builtin_bit_cast(float, __builtin_amdgcn_update_dpp(0, __builtin_bit_cast(int, v), 0x141, 0xF, 0xF, true)); }
; __device__ __forceinline__ void qk_vec(bf16_t* p, const u32x4 r, const float (&w)[8], const float (&cs)[8], const float (&sn)[8]) {
;     float x[8] = {bflo(r.x), bfhi(r.x), bflo(r.y), bfhi(r.y), bflo(r.z), bfhi(r.z), bflo(r.w), bfhi(r.w)};
;     float ss = 0.f;
; #pragma unroll
;     for (int e = 0; e < 8; ++e) ss += x[e] * x[e];
;     ss += dpp_x1(ss); ss += dpp_x2(ss); ss += dpp_hm(ss);
;     const float rstd = rsqrtf(ss * (1.f / 64.f) + NORM_EPS);
;     float o[8];
; #pragma unroll
;     for (int e = 0; e < 8; ++e) { const float y = x[e] * rstd * w[e]; o[e] = y * cs[e] + dpp_x2(y) * sn[e]; }
;     u32x4 q; q.x = pk2(o[0], o[1]); q.y = pk2(o[2], o[3]); q.z = pk2(o[4], o[5]); q.w = pk2(o[6], o[7]);
;     *(u32x4*)p = q;
; }
	v_mov_b32_dpp v87, v85 quad_perm:[2,3,0,1] row_mask:0xf bank_mask:0xf bound_ctrl:1
	v_pk_mul_f32 v[84:85], v[76:77], v[100:101] op_sel_hi:[0,1]
	v_pk_mul_f32 v[84:85], v[110:111], v[84:85]
	v_pk_mul_f32 v[76:77], v[76:77], v[88:89] op_sel_hi:[0,1]
	v_pk_fma_f32 v[80:81], v[182:183], v[86:87], v[80:81]
	v_mov_b32_dpp v86, v84 quad_perm:[2,3,0,1] row_mask:0xf bank_mask:0xf bound_ctrl:1
	v_pk_mul_f32 v[76:77], v[196:197], v[76:77]
	v_pk_mul_f32 v[94:95], v[78:79], v[84:85]
	v_mov_b32_dpp v87, v85 quad_perm:[2,3,0,1] row_mask:0xf bank_mask:0xf bound_ctrl:1
	v_mov_b32_dpp v88, v76 quad_perm:[2,3,0,1] row_mask:0xf bank_mask:0xf bound_ctrl:1
	v_pk_fma_f32 v[84:85], v[180:181], v[86:87], v[94:95]
	v_pk_mul_f32 v[86:87], v[190:191], v[76:77]
	v_mov_b32_dpp v89, v77 quad_perm:[2,3,0,1] row_mask:0xf bank_mask:0xf bound_ctrl:1
	v_pk_fma_f32 v[76:77], v[186:187], v[88:89], v[86:87]
	v_bfe_u32 v71, v81, 16, 1
	v_bfe_u32 v67, v77, 16, 1
	v_bfe_u32 v69, v76, 16, 1
	v_add3_u32 v71, v81, v71, s23
	v_bfe_u32 v81, v85, 16, 1
	v_bfe_u32 v75, v80, 16, 1
	v_add3_u32 v69, v76, v69, s23
	v_add3_u32 v67, v77, v67, s23
	v_bfe_u32 v76, v27, 16, 1
	v_bfe_u32 v77, v84, 16, 1
	v_add3_u32 v81, v85, v81, s23
	v_add3_u32 v80, v80, v75, s23
	v_bfe_u32 v75, v26, 16, 1
	v_add3_u32 v77, v84, v77, s23
	v_add3_u32 v27, v27, v76, s23
	v_lshrrev_b32_e32 v76, 16, v81
	v_add3_u32 v26, v26, v75, s23
	v_lshrrev_b32_e32 v75, 16, v77
	v_and_or_b32 v77, v67, s95, v76
	v_mul_f32_e32 v67, 0x4b800000, v74
	v_cmp_gt_f32_e32 vcc, s66, v74
	v_lshrrev_b32_e32 v26, 16, v26
	v_lshrrev_b32_e32 v27, 16, v27
	v_cndmask_b32_e32 v67, v74, v67, vcc
	v_rsq_f32_e32 v67, v67
	v_and_or_b32 v74, v80, s95, v26
	v_and_or_b32 v76, v69, s95, v75
	v_and_or_b32 v75, v71, s95, v27
	v_mul_f32_e32 v26, 0x45800000, v67
	v_cndmask_b32_e32 v26, v67, v26, vcc
	global_store_dwordx4 v[162:163], v[74:77], off offset:3072 nt
	v_pk_mul_f32 v[80:81], v[26:27], v[108:109] op_sel_hi:[0,1]
	v_pk_mul_f32 v[80:81], v[16:17], v[80:81]
	v_pk_mul_f32 v[74:75], v[26:27], v[106:107] op_sel_hi:[0,1]
	v_pk_mul_f32 v[74:75], v[20:21], v[74:75]
	v_mov_b32_dpp v84, v80 quad_perm:[2,3,0,1] row_mask:0xf bank_mask:0xf bound_ctrl:1
	v_pk_mul_f32 v[86:87], v[82:83], v[74:75]
	v_mov_b32_dpp v76, v74 quad_perm:[2,3,0,1] row_mask:0xf bank_mask:0xf bound_ctrl:1
	v_mov_b32_dpp v77, v75 quad_perm:[2,3,0,1] row_mask:0xf bank_mask:0xf bound_ctrl:1
	v_pk_fma_f32 v[74:75], v[184:185], v[76:77], v[86:87]
	v_pk_mul_f32 v[76:77], v[188:189], v[80:81]
	v_mov_b32_dpp v85, v81 quad_perm:[2,3,0,1] row_mask:0xf bank_mask:0xf bound_ctrl:1
	v_pk_mul_f32 v[80:81], v[26:27], v[114:115] op_sel_hi:[0,1]
	v_pk_mul_f32 v[80:81], v[12:13], v[80:81]
	v_pk_mul_f32 v[26:27], v[26:27], v[116:117] op_sel_hi:[0,1]
	v_pk_fma_f32 v[76:77], v[182:183], v[84:85], v[76:77]
	v_mov_b32_dpp v84, v80 quad_perm:[2,3,0,1] row_mask:0xf bank_mask:0xf bound_ctrl:1
	v_pk_mul_f32 v[26:27], v[8:9], v[26:27]
	v_pk_mul_f32 v[88:89], v[78:79], v[80:81]
	v_mov_b32_dpp v85, v81 quad_perm:[2,3,0,1] row_mask:0xf bank_mask:0xf bound_ctrl:1
	v_mov_b32_dpp v86, v26 quad_perm:[2,3,0,1] row_mask:0xf bank_mask:0xf bound_ctrl:1
	v_pk_fma_f32 v[80:81], v[180:181], v[84:85], v[88:89]
	v_pk_mul_f32 v[84:85], v[190:191], v[26:27]
	v_mov_b32_dpp v87, v27 quad_perm:[2,3,0,1] row_mask:0xf bank_mask:0xf bound_ctrl:1
	v_pk_fma_f32 v[26:27], v[186:187], v[86:87], v[84:85]
	v_bfe_u32 v84, v76, 16, 1
	v_bfe_u32 v67, v27, 16, 1
	v_add3_u32 v84, v76, v84, s23
	v_bfe_u32 v76, v80, 16, 1
	v_bfe_u32 v69, v26, 16, 1
	v_add3_u32 v27, v27, v67, s23
	v_bfe_u32 v67, v74, 16, 1
	v_add3_u32 v76, v80, v76, s23
	v_bfe_u32 v71, v77, 16, 1
	v_add3_u32 v26, v26, v69, s23
	v_add3_u32 v67, v74, v67, s23
	v_lshrrev_b32_e32 v74, 16, v76
	v_add3_u32 v71, v77, v71, s23
	v_bfe_u32 v77, v81, 16, 1
	v_and_or_b32 v76, v26, s95, v74
	v_lshlrev_b32_e32 v26, 16, v62
	v_and_b32_e32 v62, 0xffff0000, v62
	v_and_b32_e32 v100, 0xffff0000, v58
	v_bfe_u32 v69, v75, 16, 1
	v_add3_u32 v77, v81, v77, s23
	v_mov_b32_e32 v80, v26
	v_mov_b32_e32 v81, v62
	v_and_b32_e32 v101, 0xffff0000, v59
	v_mov_b32_e32 v58, v96
	v_mov_b32_e32 v59, v100
	v_add3_u32 v69, v75, v69, s23
	v_lshrrev_b32_e32 v75, 16, v77
	v_pk_mul_f32 v[80:81], v[80:81], v[80:81]
	v_pk_mul_f32 v[58:59], v[58:59], v[58:59]
	v_lshrrev_b32_e32 v67, 16, v67
	v_and_or_b32 v77, v27, s95, v75
	v_lshlrev_b32_e32 v27, 16, v63
	v_and_b32_e32 v63, 0xffff0000, v63
	v_mov_b32_e32 v102, v58
	v_mov_b32_e32 v103, v80
	v_mov_b32_e32 v80, v59
	v_and_or_b32 v74, v84, s95, v67
	v_mov_b32_e32 v84, v63
	v_mov_b32_e32 v85, v27
	v_pk_add_f32 v[58:59], v[102:103], v[80:81]
	v_mov_b32_e32 v80, v101
	v_mov_b32_e32 v81, v97
	v_pk_mul_f32 v[84:85], v[84:85], v[84:85]
	v_lshlrev_b32_e32 v86, 16, v64
	v_and_b32_e32 v64, 0xffff0000, v64
	v_pk_mul_f32 v[80:81], v[80:81], v[80:81]
	v_lshlrev_b32_e32 v102, 16, v60
	v_mov_b32_e32 v88, v64
	v_mov_b32_e32 v89, v86
	v_lshlrev_b32_e32 v103, 16, v61
	v_mov_b32_e32 v60, v104
	v_mov_b32_e32 v61, v102
	v_mov_b32_e32 v108, v81
	v_mov_b32_e32 v109, v85
	v_lshlrev_b32_e32 v87, 16, v65
	v_and_b32_e32 v65, 0xffff0000, v65
	v_pk_mul_f32 v[88:89], v[88:89], v[88:89]
	v_pk_mul_f32 v[60:61], v[60:61], v[60:61]
	v_pk_add_f32 v[58:59], v[108:109], v[58:59]
	v_mov_b32_e32 v81, v84
	v_mov_b32_e32 v94, v65
	v_mov_b32_e32 v95, v87
	v_mov_b32_e32 v106, v105
	v_mov_b32_e32 v107, v103
	v_pk_add_f32 v[58:59], v[80:81], v[58:59]
	v_mov_b32_e32 v80, v61
	v_mov_b32_e32 v81, v89
	v_pk_mul_f32 v[94:95], v[94:95], v[94:95]
	v_pk_mul_f32 v[106:107], v[106:107], v[106:107]
	v_pk_add_f32 v[58:59], v[80:81], v[58:59]
	v_mov_b32_e32 v61, v88
	v_pk_add_f32 v[58:59], v[60:61], v[58:59]
	v_mov_b32_e32 v60, v107
; __device__ __forceinline__ unsigned pk2(float lo, float hi) { return f2bf(lo) | (f2bf(hi) << 16); }
; __device__ __forceinline__ float dpp_x1(float v) { return __builtin_bit_cast(float, __builtin_amdgcn_update_dpp(0, __builtin_bit_cast(int, v), 0xB1, 0xF, 0xF, true)); }
; __device__ __forceinline__ float dpp_x2(float v) { return __builtin_bit_cast(float, __builtin_amdgcn_update_dpp(0, __builtin_bit_cast(int, v), 0x4E, 0xF, 0xF, true)); }
; __device__ __forceinline__ float dpp_hm(float v) { return __builtin_bit_cast(float, __builtin_amdgcn_update_dpp(0, __builtin_bit_cast(int, v), 0x141, 0xF, 0xF, true)); }
; __device__ __forceinline__ void qk_vec(bf16_t* p, const u32x4 r, const float (&w)[8], const float (&cs)[8], const float (&sn)[8]) {
;     float x[8] = {bflo(r.x), bfhi(r.x), bflo(r.y), bfhi(r.y), bflo(r.z), bfhi(r.z), bflo(r.w), bfhi(r.w)};
;     float ss = 0.f;
; #pragma unroll
;     for (int e = 0; e < 8; ++e) ss += x[e] * x[e];
;     ss += dpp_x1(ss); ss += dpp_x2(ss); ss += dpp_hm(ss);
;     const float rstd = rsqrtf(ss * (1.f / 64.f) + NORM_EPS);
;     float o[8];
; #pragma unroll
;     for (int e = 0; e < 8; ++e) { const float y = x[e] * rstd * w[e]; o[e] = y * cs[e] + dpp_x2(y) * sn[e]; }
;     u32x4 q; q.x = pk2(o[0], o[1]); q.y = pk2(o[2], o[3]); q.z = pk2(o[4], o[5]); q.w = pk2(o[6], o[7]);
;     *(u32x4*)p = q;
; }
	v_mov_b32_e32 v61, v95
	v_pk_add_f32 v[58:59], v[60:61], v[58:59]
	v_mov_b32_e32 v107, v94
	v_pk_add_f32 v[58:59], v[106:107], v[58:59]
	v_lshrrev_b32_e32 v69, 16, v69
	v_and_or_b32 v75, v71, s95, v69
	v_mov_b32_dpp v61, v59 quad_perm:[1,0,3,2] row_mask:0xf bank_mask:0xf bound_ctrl:1
	v_mov_b32_dpp v60, v58 quad_perm:[1,0,3,2] row_mask:0xf bank_mask:0xf bound_ctrl:1
	v_pk_add_f32 v[58:59], v[58:59], v[60:61]
	global_store_dwordx4 v[220:221], v[74:77], off nt
	v_mov_b32_e32 v71, v72
	v_mov_b32_dpp v61, v59 quad_perm:[2,3,0,1] row_mask:0xf bank_mask:0xf bound_ctrl:1
	v_mov_b32_dpp v60, v58 quad_perm:[2,3,0,1] row_mask:0xf bank_mask:0xf bound_ctrl:1
	v_pk_add_f32 v[58:59], v[58:59], v[60:61]
	v_and_b32_e32 v80, 0xffff0000, v52
	v_and_b32_e32 v81, 0xffff0000, v53
	v_mov_b32_dpp v61, v59 row_half_mirror row_mask:0xf bank_mask:0xf bound_ctrl:1
	v_mov_b32_dpp v60, v58 row_half_mirror row_mask:0xf bank_mask:0xf bound_ctrl:1
	v_pk_add_f32 v[58:59], v[58:59], v[60:61]
	s_nop 0
	v_pk_fma_f32 v[58:59], v[58:59], s[8:9], v[92:93] op_sel_hi:[1,0,0]
	s_nop 0
	v_mul_f32_e32 v60, 0x4b800000, v59
	v_cmp_gt_f32_e32 vcc, s66, v59
	s_nop 1
	v_cndmask_b32_e32 v59, v59, v60, vcc
	v_rsq_f32_e32 v59, v59
	s_nop 0
	v_mul_f32_e32 v60, 0x45800000, v59
	v_cndmask_b32_e32 v60, v59, v60, vcc
	v_pk_mul_f32 v[26:27], v[60:61], v[26:27] op_sel_hi:[0,1]
	v_pk_mul_f32 v[26:27], v[90:91], v[26:27]
	v_pk_mul_f32 v[62:63], v[60:61], v[62:63] op_sel_hi:[0,1]
	v_pk_mul_f32 v[62:63], v[36:37], v[62:63]
	v_mov_b32_dpp v72, v26 quad_perm:[2,3,0,1] row_mask:0xf bank_mask:0xf bound_ctrl:1
	v_pk_mul_f32 v[76:77], v[82:83], v[26:27]
	v_mov_b32_dpp v73, v27 quad_perm:[2,3,0,1] row_mask:0xf bank_mask:0xf bound_ctrl:1
	v_mov_b32_dpp v74, v62 quad_perm:[2,3,0,1] row_mask:0xf bank_mask:0xf bound_ctrl:1
	v_pk_fma_f32 v[26:27], v[184:185], v[72:73], v[76:77]
	v_pk_mul_f32 v[72:73], v[188:189], v[62:63]
	v_mov_b32_dpp v75, v63 quad_perm:[2,3,0,1] row_mask:0xf bank_mask:0xf bound_ctrl:1
	v_pk_fma_f32 v[62:63], v[182:183], v[74:75], v[72:73]
	v_pk_mul_f32 v[72:73], v[60:61], v[86:87] op_sel_hi:[0,1]
	v_pk_mul_f32 v[72:73], v[34:35], v[72:73]
	v_pk_mul_f32 v[60:61], v[60:61], v[64:65] op_sel_hi:[0,1]
	v_pk_mul_f32 v[60:61], v[28:29], v[60:61]
	v_mov_b32_dpp v74, v72 quad_perm:[2,3,0,1] row_mask:0xf bank_mask:0xf bound_ctrl:1
	v_pk_mul_f32 v[76:77], v[78:79], v[72:73]
	v_mov_b32_dpp v75, v73 quad_perm:[2,3,0,1] row_mask:0xf bank_mask:0xf bound_ctrl:1
	v_mov_b32_dpp v64, v60 quad_perm:[2,3,0,1] row_mask:0xf bank_mask:0xf bound_ctrl:1
	v_pk_fma_f32 v[72:73], v[180:181], v[74:75], v[76:77]
	v_pk_mul_f32 v[74:75], v[190:191], v[60:61]
	v_mov_b32_dpp v65, v61 quad_perm:[2,3,0,1] row_mask:0xf bank_mask:0xf bound_ctrl:1
	v_pk_fma_f32 v[60:61], v[186:187], v[64:65], v[74:75]
	v_bfe_u32 v67, v62, 16, 1
	v_bfe_u32 v59, v61, 16, 1
	v_add3_u32 v62, v62, v67, s23
	v_bfe_u32 v67, v73, 16, 1
	v_bfe_u32 v65, v63, 16, 1
	v_add3_u32 v59, v61, v59, s23
	v_bfe_u32 v61, v26, 16, 1
	v_add3_u32 v67, v73, v67, s23
	v_bfe_u32 v64, v60, 16, 1
	v_add3_u32 v63, v63, v65, s23
	v_bfe_u32 v65, v72, 16, 1
	v_add3_u32 v26, v26, v61, s23
	v_lshrrev_b32_e32 v61, 16, v67
	v_add3_u32 v60, v60, v64, s23
	v_bfe_u32 v64, v27, 16, 1
	v_add3_u32 v65, v72, v65, s23
	v_and_or_b32 v61, v59, s95, v61
	v_mul_f32_e32 v59, 0x4b800000, v58
	v_cmp_gt_f32_e32 vcc, s66, v58
	v_add3_u32 v27, v27, v64, s23
	v_lshrrev_b32_e32 v64, 16, v65
	v_cndmask_b32_e32 v58, v58, v59, vcc
	v_and_or_b32 v60, v60, s95, v64
	v_rsq_f32_e32 v64, v58
	v_lshrrev_b32_e32 v26, 16, v26
	v_lshrrev_b32_e32 v27, 16, v27
	v_and_or_b32 v58, v62, s95, v26
	v_mul_f32_e32 v26, 0x45800000, v64
	v_and_or_b32 v59, v63, s95, v27
	v_cndmask_b32_e32 v26, v64, v26, vcc
	global_store_dwordx4 v[218:219], v[58:61], off nt
	v_pk_mul_f32 v[62:63], v[26:27], v[100:101] op_sel_hi:[0,1]
	v_pk_mul_f32 v[62:63], v[112:113], v[62:63]
	v_pk_mul_f32 v[58:59], v[26:27], v[96:97] op_sel_hi:[0,1]
	v_pk_mul_f32 v[58:59], v[98:99], v[58:59]
	v_mov_b32_dpp v64, v62 quad_perm:[2,3,0,1] row_mask:0xf bank_mask:0xf bound_ctrl:1
	v_pk_mul_f32 v[72:73], v[70:71], v[58:59]
	v_mov_b32_dpp v60, v58 quad_perm:[2,3,0,1] row_mask:0xf bank_mask:0xf bound_ctrl:1
	v_mov_b32_dpp v61, v59 quad_perm:[2,3,0,1] row_mask:0xf bank_mask:0xf bound_ctrl:1
	v_pk_fma_f32 v[58:59], v[170:171], v[60:61], v[72:73]
	v_pk_mul_f32 v[60:61], v[176:177], v[62:63]
	v_mov_b32_dpp v65, v63 quad_perm:[2,3,0,1] row_mask:0xf bank_mask:0xf bound_ctrl:1
	v_pk_mul_f32 v[62:63], v[26:27], v[102:103] op_sel_hi:[0,1]
	v_pk_mul_f32 v[62:63], v[110:111], v[62:63]
	v_pk_mul_f32 v[26:27], v[26:27], v[104:105] op_sel_hi:[0,1]
	v_mov_b32_e32 v67, v68
	v_pk_fma_f32 v[60:61], v[168:169], v[64:65], v[60:61]
	v_mov_b32_dpp v64, v62 quad_perm:[2,3,0,1] row_mask:0xf bank_mask:0xf bound_ctrl:1
	v_pk_mul_f32 v[26:27], v[196:197], v[26:27]
	v_pk_mul_f32 v[68:69], v[66:67], v[62:63]
	v_mov_b32_dpp v65, v63 quad_perm:[2,3,0,1] row_mask:0xf bank_mask:0xf bound_ctrl:1
	v_mov_b32_dpp v72, v26 quad_perm:[2,3,0,1] row_mask:0xf bank_mask:0xf bound_ctrl:1
	v_pk_fma_f32 v[62:63], v[166:167], v[64:65], v[68:69]
	v_pk_mul_f32 v[64:65], v[174:175], v[26:27]
	v_mov_b32_dpp v73, v27 quad_perm:[2,3,0,1] row_mask:0xf bank_mask:0xf bound_ctrl:1
	v_pk_fma_f32 v[26:27], v[172:173], v[72:73], v[64:65]
	v_bfe_u32 v69, v60, 16, 1
	v_bfe_u32 v64, v27, 16, 1
	v_add3_u32 v86, v60, v69, s23
	v_add3_u32 v27, v27, v64, s23
	v_bfe_u32 v60, v58, 16, 1
	v_bfe_u32 v64, v62, 16, 1
	v_bfe_u32 v65, v26, 16, 1
	v_add3_u32 v62, v62, v64, s23
	v_add3_u32 v58, v58, v60, s23
	v_bfe_u32 v68, v61, 16, 1
	v_add3_u32 v26, v26, v65, s23
	v_lshrrev_b32_e32 v88, 16, v58
	v_lshrrev_b32_e32 v58, 16, v62
; __device__ __forceinline__ unsigned pk2(float lo, float hi) { return f2bf(lo) | (f2bf(hi) << 16); }
; __device__ __forceinline__ float dpp_x1(float v) { return __builtin_bit_cast(float, __builtin_amdgcn_update_dpp(0, __builtin_bit_cast(int, v), 0xB1, 0xF, 0xF, true)); }
; __device__ __forceinline__ float dpp_x2(float v) { return __builtin_bit_cast(float, __builtin_amdgcn_update_dpp(0, __builtin_bit_cast(int, v), 0x4E, 0xF, 0xF, true)); }
; __device__ __forceinline__ float dpp_hm(float v) { return __builtin_bit_cast(float, __builtin_amdgcn_update_dpp(0, __builtin_bit_cast(int, v), 0x141, 0xF, 0xF, true)); }
; __device__ __forceinline__ void qk_vec(bf16_t* p, const u32x4 r, const float (&w)[8], const float (&cs)[8], const float (&sn)[8]) {
;     float x[8] = {bflo(r.x), bfhi(r.x), bflo(r.y), bfhi(r.y), bflo(r.z), bfhi(r.z), bflo(r.w), bfhi(r.w)};
;     float ss = 0.f;
; #pragma unroll
;     for (int e = 0; e < 8; ++e) ss += x[e] * x[e];
;     ss += dpp_x1(ss); ss += dpp_x2(ss); ss += dpp_hm(ss);
;     const float rstd = rsqrtf(ss * (1.f / 64.f) + NORM_EPS);
;     float o[8];
; #pragma unroll
;     for (int e = 0; e < 8; ++e) { const float y = x[e] * rstd * w[e]; o[e] = y * cs[e] + dpp_x2(y) * sn[e]; }
;     u32x4 q; q.x = pk2(o[0], o[1]); q.y = pk2(o[2], o[3]); q.z = pk2(o[4], o[5]); q.w = pk2(o[6], o[7]);
;     *(u32x4*)p = q;
; }
	v_add3_u32 v87, v61, v68, s23
	v_bfe_u32 v61, v59, 16, 1
	v_bfe_u32 v65, v63, 16, 1
	v_and_or_b32 v58, v26, s95, v58
	v_lshlrev_b32_e32 v26, 16, v54
	v_and_b32_e32 v54, 0xffff0000, v54
	v_lshlrev_b32_e32 v74, 16, v50
	v_and_b32_e32 v76, 0xffff0000, v50
	v_add3_u32 v63, v63, v65, s23
	v_add3_u32 v59, v59, v61, s23
	v_mov_b32_e32 v60, v26
	v_mov_b32_e32 v61, v54
	v_lshlrev_b32_e32 v75, 16, v51
	v_and_b32_e32 v77, 0xffff0000, v51
	v_mov_b32_e32 v50, v74
	v_mov_b32_e32 v51, v76
	v_lshrrev_b32_e32 v89, 16, v59
	v_lshrrev_b32_e32 v59, 16, v63
	v_pk_mul_f32 v[60:61], v[60:61], v[60:61]
	v_pk_mul_f32 v[50:51], v[50:51], v[50:51]
	v_and_or_b32 v59, v27, s95, v59
	v_lshlrev_b32_e32 v27, 16, v55
	v_and_b32_e32 v55, 0xffff0000, v55
	v_mov_b32_e32 v78, v50
	v_mov_b32_e32 v79, v60
	v_mov_b32_e32 v60, v51
	v_mov_b32_e32 v62, v55
	v_mov_b32_e32 v63, v27
	v_pk_add_f32 v[50:51], v[78:79], v[60:61]
	v_mov_b32_e32 v60, v77
	v_mov_b32_e32 v61, v75
	v_pk_mul_f32 v[62:63], v[62:63], v[62:63]
	v_lshlrev_b32_e32 v64, 16, v56
	v_and_b32_e32 v68, 0xffff0000, v56
	v_pk_mul_f32 v[60:61], v[60:61], v[60:61]
	v_lshlrev_b32_e32 v78, 16, v52
	v_lshlrev_b32_e32 v65, 16, v57
	v_and_b32_e32 v69, 0xffff0000, v57
	v_mov_b32_e32 v56, v68
	v_mov_b32_e32 v57, v64
	v_lshlrev_b32_e32 v79, 16, v53
	v_mov_b32_e32 v52, v80
	v_mov_b32_e32 v53, v78
	v_mov_b32_e32 v84, v61
	v_mov_b32_e32 v85, v63
	v_pk_mul_f32 v[56:57], v[56:57], v[56:57]
	v_pk_mul_f32 v[52:53], v[52:53], v[52:53]
	v_pk_add_f32 v[50:51], v[84:85], v[50:51]
	v_mov_b32_e32 v61, v62
	v_mov_b32_e32 v72, v69
	v_mov_b32_e32 v73, v65
	v_mov_b32_e32 v82, v81
	v_mov_b32_e32 v83, v79
	v_pk_add_f32 v[50:51], v[60:61], v[50:51]
	v_mov_b32_e32 v60, v53
	v_mov_b32_e32 v61, v57
	v_pk_mul_f32 v[72:73], v[72:73], v[72:73]
	v_pk_mul_f32 v[82:83], v[82:83], v[82:83]
	v_pk_add_f32 v[50:51], v[60:61], v[50:51]
	v_mov_b32_e32 v53, v56
	v_pk_add_f32 v[50:51], v[52:53], v[50:51]
	v_mov_b32_e32 v52, v83
	v_mov_b32_e32 v53, v73
	v_pk_add_f32 v[50:51], v[52:53], v[50:51]
	v_mov_b32_e32 v83, v72
	v_pk_add_f32 v[50:51], v[82:83], v[50:51]
	v_and_or_b32 v57, v87, s95, v89
	v_and_or_b32 v56, v86, s95, v88
	v_mov_b32_dpp v53, v51 quad_perm:[1,0,3,2] row_mask:0xf bank_mask:0xf bound_ctrl:1
	v_mov_b32_dpp v52, v50 quad_perm:[1,0,3,2] row_mask:0xf bank_mask:0xf bound_ctrl:1
	v_pk_add_f32 v[50:51], v[50:51], v[52:53]
	global_store_dwordx4 v[134:135], v[56:59], off offset:3072 nt
	s_nop 0
	v_mov_b32_dpp v53, v51 quad_perm:[2,3,0,1] row_mask:0xf bank_mask:0xf bound_ctrl:1
	v_mov_b32_dpp v52, v50 quad_perm:[2,3,0,1] row_mask:0xf bank_mask:0xf bound_ctrl:1
	v_pk_add_f32 v[50:51], v[50:51], v[52:53]
	s_nop 1
	v_mov_b32_dpp v53, v51 row_half_mirror row_mask:0xf bank_mask:0xf bound_ctrl:1
	v_mov_b32_dpp v52, v50 row_half_mirror row_mask:0xf bank_mask:0xf bound_ctrl:1
	v_pk_add_f32 v[50:51], v[50:51], v[52:53]
	s_nop 0
	v_pk_fma_f32 v[50:51], v[50:51], s[8:9], v[92:93] op_sel_hi:[1,0,0]
	s_nop 0
	v_mul_f32_e32 v52, 0x4b800000, v51
	v_cmp_gt_f32_e32 vcc, s66, v51
	s_nop 1
	v_cndmask_b32_e32 v51, v51, v52, vcc
	v_rsq_f32_e32 v51, v51
	s_nop 0
	v_mul_f32_e32 v52, 0x45800000, v51
	v_cndmask_b32_e32 v52, v51, v52, vcc
	v_pk_mul_f32 v[26:27], v[52:53], v[26:27] op_sel_hi:[0,1]
	v_pk_mul_f32 v[26:27], v[20:21], v[26:27]
	v_pk_mul_f32 v[54:55], v[52:53], v[54:55] op_sel_hi:[0,1]
	v_pk_mul_f32 v[54:55], v[16:17], v[54:55]
	v_mov_b32_dpp v56, v26 quad_perm:[2,3,0,1] row_mask:0xf bank_mask:0xf bound_ctrl:1
	v_pk_mul_f32 v[60:61], v[70:71], v[26:27]
	v_mov_b32_dpp v57, v27 quad_perm:[2,3,0,1] row_mask:0xf bank_mask:0xf bound_ctrl:1
	v_mov_b32_dpp v58, v54 quad_perm:[2,3,0,1] row_mask:0xf bank_mask:0xf bound_ctrl:1
	v_pk_fma_f32 v[26:27], v[170:171], v[56:57], v[60:61]
	v_pk_mul_f32 v[56:57], v[176:177], v[54:55]
	v_mov_b32_dpp v59, v55 quad_perm:[2,3,0,1] row_mask:0xf bank_mask:0xf bound_ctrl:1
	v_pk_fma_f32 v[54:55], v[168:169], v[58:59], v[56:57]
	v_pk_mul_f32 v[56:57], v[52:53], v[64:65] op_sel_hi:[0,1]
	v_pk_mul_f32 v[56:57], v[12:13], v[56:57]
	v_pk_mul_f32 v[52:53], v[52:53], v[68:69] op_sel_hi:[0,1]
	v_pk_mul_f32 v[52:53], v[8:9], v[52:53]
	v_mov_b32_dpp v58, v56 quad_perm:[2,3,0,1] row_mask:0xf bank_mask:0xf bound_ctrl:1
	v_pk_mul_f32 v[62:63], v[66:67], v[56:57]
	v_mov_b32_dpp v59, v57 quad_perm:[2,3,0,1] row_mask:0xf bank_mask:0xf bound_ctrl:1
	v_mov_b32_dpp v60, v52 quad_perm:[2,3,0,1] row_mask:0xf bank_mask:0xf bound_ctrl:1
	v_pk_fma_f32 v[56:57], v[166:167], v[58:59], v[62:63]
	v_pk_mul_f32 v[58:59], v[174:175], v[52:53]
	v_mov_b32_dpp v61, v53 quad_perm:[2,3,0,1] row_mask:0xf bank_mask:0xf bound_ctrl:1
	v_pk_fma_f32 v[52:53], v[172:173], v[60:61], v[58:59]
	v_bfe_u32 v60, v54, 16, 1
	v_bfe_u32 v51, v53, 16, 1
	v_add3_u32 v54, v54, v60, s23
	v_bfe_u32 v60, v57, 16, 1
	v_bfe_u32 v59, v55, 16, 1
	v_add3_u32 v51, v53, v51, s23
	v_bfe_u32 v53, v26, 16, 1
	v_add3_u32 v57, v57, v60, s23
	v_add3_u32 v55, v55, v59, s23
	v_bfe_u32 v59, v56, 16, 1
	v_add3_u32 v26, v26, v53, s23
	v_lshrrev_b32_e32 v53, 16, v57
	v_bfe_u32 v58, v52, 16, 1
	v_add3_u32 v56, v56, v59, s23
	v_and_or_b32 v53, v51, s95, v53
	v_mul_f32_e32 v51, 0x4b800000, v50
	v_cmp_gt_f32_e32 vcc, s66, v50
	v_add3_u32 v52, v52, v58, s23
	v_lshrrev_b32_e32 v56, 16, v56
	v_cndmask_b32_e32 v50, v50, v51, vcc
	v_and_or_b32 v52, v52, s95, v56
	v_rsq_f32_e32 v56, v50
	v_bfe_u32 v58, v27, 16, 1
	v_add3_u32 v27, v27, v58, s23
	v_lshrrev_b32_e32 v26, 16, v26
	v_lshrrev_b32_e32 v27, 16, v27
	v_and_or_b32 v50, v54, s95, v26
	v_mul_f32_e32 v26, 0x45800000, v56
	v_and_or_b32 v51, v55, s95, v27
	v_cndmask_b32_e32 v26, v56, v26, vcc
	global_store_dwordx4 v[216:217], v[50:53], off nt
	v_pk_mul_f32 v[54:55], v[26:27], v[76:77] op_sel_hi:[0,1]
; __device__ __forceinline__ unsigned pk2(float lo, float hi) { return f2bf(lo) | (f2bf(hi) << 16); }
; __device__ __forceinline__ float dpp_x1(float v) { return __builtin_bit_cast(float, __builtin_amdgcn_update_dpp(0, __builtin_bit_cast(int, v), 0xB1, 0xF, 0xF, true)); }
; __device__ __forceinline__ float dpp_x2(float v) { return __builtin_bit_cast(float, __builtin_amdgcn_update_dpp(0, __builtin_bit_cast(int, v), 0x4E, 0xF, 0xF, true)); }
; __device__ __forceinline__ float dpp_hm(float v) { return __builtin_bit_cast(float, __builtin_amdgcn_update_dpp(0, __builtin_bit_cast(int, v), 0x141, 0xF, 0xF, true)); }
; __device__ __forceinline__ void qk_vec(bf16_t* p, const u32x4 r, const float (&w)[8], const float (&cs)[8], const float (&sn)[8]) {
;     float x[8] = {bflo(r.x), bfhi(r.x), bflo(r.y), bfhi(r.y), bflo(r.z), bfhi(r.z), bflo(r.w), bfhi(r.w)};
;     float ss = 0.f;
; #pragma unroll
;     for (int e = 0; e < 8; ++e) ss += x[e] * x[e];
;     ss += dpp_x1(ss); ss += dpp_x2(ss); ss += dpp_hm(ss);
;     const float rstd = rsqrtf(ss * (1.f / 64.f) + NORM_EPS);
;     float o[8];
; #pragma unroll
;     for (int e = 0; e < 8; ++e) { const float y = x[e] * rstd * w[e]; o[e] = y * cs[e] + dpp_x2(y) * sn[e]; }
;     u32x4 q; q.x = pk2(o[0], o[1]); q.y = pk2(o[2], o[3]); q.z = pk2(o[4], o[5]); q.w = pk2(o[6], o[7]);
;     *(u32x4*)p = q;
; }
	v_pk_mul_f32 v[54:55], v[36:37], v[54:55]
	v_pk_mul_f32 v[50:51], v[26:27], v[74:75] op_sel_hi:[0,1]
	v_pk_mul_f32 v[50:51], v[90:91], v[50:51]
	v_mov_b32_dpp v56, v54 quad_perm:[2,3,0,1] row_mask:0xf bank_mask:0xf bound_ctrl:1
	v_pk_mul_f32 v[58:59], v[70:71], v[50:51]
	v_mov_b32_dpp v52, v50 quad_perm:[2,3,0,1] row_mask:0xf bank_mask:0xf bound_ctrl:1
	v_mov_b32_dpp v53, v51 quad_perm:[2,3,0,1] row_mask:0xf bank_mask:0xf bound_ctrl:1
	v_pk_fma_f32 v[50:51], v[170:171], v[52:53], v[58:59]
	v_pk_mul_f32 v[52:53], v[176:177], v[54:55]
	v_mov_b32_dpp v57, v55 quad_perm:[2,3,0,1] row_mask:0xf bank_mask:0xf bound_ctrl:1
	v_pk_mul_f32 v[54:55], v[26:27], v[78:79] op_sel_hi:[0,1]
	v_pk_mul_f32 v[54:55], v[34:35], v[54:55]
	v_pk_mul_f32 v[26:27], v[26:27], v[80:81] op_sel_hi:[0,1]
	v_pk_fma_f32 v[52:53], v[168:169], v[56:57], v[52:53]
	v_mov_b32_dpp v56, v54 quad_perm:[2,3,0,1] row_mask:0xf bank_mask:0xf bound_ctrl:1
	v_pk_mul_f32 v[26:27], v[28:29], v[26:27]
	v_pk_mul_f32 v[60:61], v[66:67], v[54:55]
	v_mov_b32_dpp v57, v55 quad_perm:[2,3,0,1] row_mask:0xf bank_mask:0xf bound_ctrl:1
	v_mov_b32_dpp v58, v26 quad_perm:[2,3,0,1] row_mask:0xf bank_mask:0xf bound_ctrl:1
	v_pk_fma_f32 v[54:55], v[166:167], v[56:57], v[60:61]
	v_pk_mul_f32 v[56:57], v[174:175], v[26:27]
	v_mov_b32_dpp v59, v27 quad_perm:[2,3,0,1] row_mask:0xf bank_mask:0xf bound_ctrl:1
	v_pk_fma_f32 v[26:27], v[172:173], v[58:59], v[56:57]
	v_bfe_u32 v59, v52, 16, 1
	v_bfe_u32 v56, v27, 16, 1
	v_add3_u32 v74, v52, v59, s23
	v_add3_u32 v27, v27, v56, s23
	v_bfe_u32 v52, v50, 16, 1
	v_bfe_u32 v56, v54, 16, 1
	v_bfe_u32 v57, v26, 16, 1
	v_add3_u32 v54, v54, v56, s23
	v_add3_u32 v50, v50, v52, s23
	v_bfe_u32 v58, v53, 16, 1
	v_add3_u32 v26, v26, v57, s23
	v_lshrrev_b32_e32 v76, 16, v50
	v_lshrrev_b32_e32 v50, 16, v54
	v_add3_u32 v75, v53, v58, s23
	v_bfe_u32 v53, v51, 16, 1
	v_bfe_u32 v57, v55, 16, 1
	v_and_or_b32 v50, v26, s95, v50
	v_lshlrev_b32_e32 v26, 16, v46
	v_and_b32_e32 v46, 0xffff0000, v46
	v_lshlrev_b32_e32 v62, 16, v42
	v_and_b32_e32 v64, 0xffff0000, v42
	v_add3_u32 v55, v55, v57, s23
	v_add3_u32 v51, v51, v53, s23
	v_mov_b32_e32 v52, v26
	v_mov_b32_e32 v53, v46
	v_lshlrev_b32_e32 v63, 16, v43
	v_and_b32_e32 v65, 0xffff0000, v43
	v_mov_b32_e32 v42, v62
	v_mov_b32_e32 v43, v64
	v_lshrrev_b32_e32 v77, 16, v51
	v_lshrrev_b32_e32 v51, 16, v55
	v_pk_mul_f32 v[52:53], v[52:53], v[52:53]
	v_pk_mul_f32 v[42:43], v[42:43], v[42:43]
	v_and_or_b32 v51, v27, s95, v51
	v_lshlrev_b32_e32 v27, 16, v47
	v_and_b32_e32 v47, 0xffff0000, v47
	v_mov_b32_e32 v66, v42
	v_mov_b32_e32 v67, v52
	v_mov_b32_e32 v52, v43
	v_mov_b32_e32 v54, v47
	v_mov_b32_e32 v55, v27
	v_pk_add_f32 v[42:43], v[66:67], v[52:53]
	v_mov_b32_e32 v52, v65
	v_mov_b32_e32 v53, v63
	v_pk_mul_f32 v[54:55], v[54:55], v[54:55]
	v_lshlrev_b32_e32 v56, 16, v48
	v_and_b32_e32 v58, 0xffff0000, v48
	v_pk_mul_f32 v[52:53], v[52:53], v[52:53]
	v_lshlrev_b32_e32 v66, 16, v44
	v_and_b32_e32 v68, 0xffff0000, v44
	v_lshlrev_b32_e32 v57, 16, v49
	v_and_b32_e32 v59, 0xffff0000, v49
	v_mov_b32_e32 v48, v58
	v_mov_b32_e32 v49, v56
	v_lshlrev_b32_e32 v67, 16, v45
	v_and_b32_e32 v69, 0xffff0000, v45
	v_mov_b32_e32 v44, v68
	v_mov_b32_e32 v45, v66
	v_mov_b32_e32 v72, v53
	v_mov_b32_e32 v73, v55
	v_pk_mul_f32 v[48:49], v[48:49], v[48:49]
	v_pk_mul_f32 v[44:45], v[44:45], v[44:45]
	v_pk_add_f32 v[42:43], v[72:73], v[42:43]
	v_mov_b32_e32 v53, v54
	v_mov_b32_e32 v60, v59
	v_mov_b32_e32 v61, v57
	v_mov_b32_e32 v70, v69
	v_mov_b32_e32 v71, v67
	v_pk_add_f32 v[42:43], v[52:53], v[42:43]
	v_mov_b32_e32 v52, v45
	v_mov_b32_e32 v53, v49
	v_pk_mul_f32 v[60:61], v[60:61], v[60:61]
	v_pk_mul_f32 v[70:71], v[70:71], v[70:71]
	v_pk_add_f32 v[42:43], v[52:53], v[42:43]
	v_mov_b32_e32 v45, v48
	v_pk_add_f32 v[42:43], v[44:45], v[42:43]
	v_mov_b32_e32 v44, v71
	v_mov_b32_e32 v45, v61
	v_pk_add_f32 v[42:43], v[44:45], v[42:43]
	v_mov_b32_e32 v71, v60
	v_pk_add_f32 v[42:43], v[70:71], v[42:43]
	v_and_or_b32 v49, v75, s95, v77
	v_and_or_b32 v48, v74, s95, v76
	v_mov_b32_dpp v45, v43 quad_perm:[1,0,3,2] row_mask:0xf bank_mask:0xf bound_ctrl:1
	v_mov_b32_dpp v44, v42 quad_perm:[1,0,3,2] row_mask:0xf bank_mask:0xf bound_ctrl:1
	v_pk_add_f32 v[42:43], v[42:43], v[44:45]
	global_store_dwordx4 v[192:193], v[48:51], off nt
	s_nop 0
	v_mov_b32_dpp v45, v43 quad_perm:[2,3,0,1] row_mask:0xf bank_mask:0xf bound_ctrl:1
	v_mov_b32_dpp v44, v42 quad_perm:[2,3,0,1] row_mask:0xf bank_mask:0xf bound_ctrl:1
	v_pk_add_f32 v[42:43], v[42:43], v[44:45]
	s_nop 1
	v_mov_b32_dpp v45, v43 row_half_mirror row_mask:0xf bank_mask:0xf bound_ctrl:1
	v_mov_b32_dpp v44, v42 row_half_mirror row_mask:0xf bank_mask:0xf bound_ctrl:1
	v_pk_add_f32 v[42:43], v[42:43], v[44:45]
	s_nop 0
	v_pk_fma_f32 v[42:43], v[42:43], s[8:9], v[92:93] op_sel_hi:[1,0,0]
	s_nop 0
	v_mul_f32_e32 v44, 0x4b800000, v43
	v_cmp_gt_f32_e32 vcc, s66, v43
	s_nop 1
	v_cndmask_b32_e32 v43, v43, v44, vcc
	v_rsq_f32_e32 v43, v43
	s_nop 0
	v_mul_f32_e32 v44, 0x45800000, v43
	v_cndmask_b32_e32 v44, v43, v44, vcc
	v_pk_mul_f32 v[26:27], v[44:45], v[26:27] op_sel_hi:[0,1]
	v_pk_mul_f32 v[26:27], v[98:99], v[26:27]
	v_pk_mul_f32 v[46:47], v[44:45], v[46:47] op_sel_hi:[0,1]
	v_pk_mul_f32 v[46:47], v[112:113], v[46:47]
	v_mov_b32_dpp v48, v26 quad_perm:[2,3,0,1] row_mask:0xf bank_mask:0xf bound_ctrl:1
	v_pk_mul_f32 v[52:53], v[10:11], v[26:27]
	v_mov_b32_dpp v49, v27 quad_perm:[2,3,0,1] row_mask:0xf bank_mask:0xf bound_ctrl:1
	v_mov_b32_dpp v50, v46 quad_perm:[2,3,0,1] row_mask:0xf bank_mask:0xf bound_ctrl:1
	v_pk_fma_f32 v[26:27], v[142:143], v[48:49], v[52:53]
	v_pk_mul_f32 v[48:49], v[150:151], v[46:47]
; __device__ __forceinline__ unsigned pk2(float lo, float hi) { return f2bf(lo) | (f2bf(hi) << 16); }
; __device__ __forceinline__ float dpp_x1(float v) { return __builtin_bit_cast(float, __builtin_amdgcn_update_dpp(0, __builtin_bit_cast(int, v), 0xB1, 0xF, 0xF, true)); }
; __device__ __forceinline__ float dpp_x2(float v) { return __builtin_bit_cast(float, __builtin_amdgcn_update_dpp(0, __builtin_bit_cast(int, v), 0x4E, 0xF, 0xF, true)); }
; __device__ __forceinline__ float dpp_hm(float v) { return __builtin_bit_cast(float, __builtin_amdgcn_update_dpp(0, __builtin_bit_cast(int, v), 0x141, 0xF, 0xF, true)); }
; __device__ __forceinline__ void qk_vec(bf16_t* p, const u32x4 r, const float (&w)[8], const float (&cs)[8], const float (&sn)[8]) {
;     float x[8] = {bflo(r.x), bfhi(r.x), bflo(r.y), bfhi(r.y), bflo(r.z), bfhi(r.z), bflo(r.w), bfhi(r.w)};
;     float ss = 0.f;
; #pragma unroll
;     for (int e = 0; e < 8; ++e) ss += x[e] * x[e];
;     ss += dpp_x1(ss); ss += dpp_x2(ss); ss += dpp_hm(ss);
;     const float rstd = rsqrtf(ss * (1.f / 64.f) + NORM_EPS);
;     float o[8];
; #pragma unroll
;     for (int e = 0; e < 8; ++e) { const float y = x[e] * rstd * w[e]; o[e] = y * cs[e] + dpp_x2(y) * sn[e]; }
;     u32x4 q; q.x = pk2(o[0], o[1]); q.y = pk2(o[2], o[3]); q.z = pk2(o[4], o[5]); q.w = pk2(o[6], o[7]);
;     *(u32x4*)p = q;
; }
	v_mov_b32_dpp v51, v47 quad_perm:[2,3,0,1] row_mask:0xf bank_mask:0xf bound_ctrl:1
	v_pk_fma_f32 v[46:47], v[146:147], v[50:51], v[48:49]
	v_pk_mul_f32 v[48:49], v[44:45], v[56:57] op_sel_hi:[0,1]
	v_pk_mul_f32 v[48:49], v[110:111], v[48:49]
	v_pk_mul_f32 v[44:45], v[44:45], v[58:59] op_sel_hi:[0,1]
	v_pk_mul_f32 v[44:45], v[196:197], v[44:45]
	v_mov_b32_dpp v50, v48 quad_perm:[2,3,0,1] row_mask:0xf bank_mask:0xf bound_ctrl:1
	v_pk_mul_f32 v[54:55], v[6:7], v[48:49]
	v_mov_b32_dpp v51, v49 quad_perm:[2,3,0,1] row_mask:0xf bank_mask:0xf bound_ctrl:1
	v_mov_b32_dpp v52, v44 quad_perm:[2,3,0,1] row_mask:0xf bank_mask:0xf bound_ctrl:1
	v_pk_fma_f32 v[48:49], v[140:141], v[50:51], v[54:55]
	v_pk_mul_f32 v[50:51], v[148:149], v[44:45]
	v_mov_b32_dpp v53, v45 quad_perm:[2,3,0,1] row_mask:0xf bank_mask:0xf bound_ctrl:1
	v_pk_fma_f32 v[44:45], v[144:145], v[52:53], v[50:51]
	v_bfe_u32 v52, v46, 16, 1
	v_bfe_u32 v43, v45, 16, 1
	v_add3_u32 v46, v46, v52, s23
	v_bfe_u32 v52, v49, 16, 1
	v_bfe_u32 v51, v47, 16, 1
	v_add3_u32 v43, v45, v43, s23
	v_bfe_u32 v45, v26, 16, 1
	v_add3_u32 v49, v49, v52, s23
	v_add3_u32 v47, v47, v51, s23
	v_bfe_u32 v51, v48, 16, 1
	v_add3_u32 v26, v26, v45, s23
	v_lshrrev_b32_e32 v45, 16, v49
	v_bfe_u32 v50, v44, 16, 1
	v_add3_u32 v48, v48, v51, s23
	v_and_or_b32 v45, v43, s95, v45
	v_mul_f32_e32 v43, 0x4b800000, v42
	v_cmp_gt_f32_e32 vcc, s66, v42
	v_add3_u32 v44, v44, v50, s23
	v_lshrrev_b32_e32 v48, 16, v48
	v_cndmask_b32_e32 v42, v42, v43, vcc
	v_and_or_b32 v44, v44, s95, v48
	v_rsq_f32_e32 v48, v42
	v_bfe_u32 v50, v27, 16, 1
	v_add3_u32 v27, v27, v50, s23
	v_lshrrev_b32_e32 v26, 16, v26
	v_lshrrev_b32_e32 v27, 16, v27
	v_and_or_b32 v42, v46, s95, v26
	v_mul_f32_e32 v26, 0x45800000, v48
	v_and_or_b32 v43, v47, s95, v27
	v_cndmask_b32_e32 v26, v48, v26, vcc
	global_store_dwordx4 v[132:133], v[42:45], off offset:3072 nt
	s_nop 1
	v_pk_mul_f32 v[42:43], v[26:27], v[62:63] op_sel_hi:[0,1]
	v_pk_mul_f32 v[20:21], v[20:21], v[42:43]
	v_pk_mul_f32 v[44:45], v[26:27], v[64:65] op_sel_hi:[0,1]
	v_pk_mul_f32 v[16:17], v[16:17], v[44:45]
	v_mov_b32_dpp v42, v20 quad_perm:[2,3,0,1] row_mask:0xf bank_mask:0xf bound_ctrl:1
	v_pk_mul_f32 v[46:47], v[10:11], v[20:21]
	v_mov_b32_dpp v43, v21 quad_perm:[2,3,0,1] row_mask:0xf bank_mask:0xf bound_ctrl:1
	v_mov_b32_dpp v44, v16 quad_perm:[2,3,0,1] row_mask:0xf bank_mask:0xf bound_ctrl:1
	v_pk_fma_f32 v[20:21], v[142:143], v[42:43], v[46:47]
	v_pk_mul_f32 v[42:43], v[150:151], v[16:17]
	v_mov_b32_dpp v45, v17 quad_perm:[2,3,0,1] row_mask:0xf bank_mask:0xf bound_ctrl:1
	v_pk_fma_f32 v[16:17], v[146:147], v[44:45], v[42:43]
	v_pk_mul_f32 v[42:43], v[26:27], v[66:67] op_sel_hi:[0,1]
	v_pk_mul_f32 v[12:13], v[12:13], v[42:43]
	v_pk_mul_f32 v[26:27], v[26:27], v[68:69] op_sel_hi:[0,1]
	v_pk_mul_f32 v[8:9], v[8:9], v[26:27]
	v_mov_b32_dpp v42, v12 quad_perm:[2,3,0,1] row_mask:0xf bank_mask:0xf bound_ctrl:1
	v_pk_mul_f32 v[44:45], v[6:7], v[12:13]
	v_mov_b32_dpp v43, v13 quad_perm:[2,3,0,1] row_mask:0xf bank_mask:0xf bound_ctrl:1
	v_mov_b32_dpp v26, v8 quad_perm:[2,3,0,1] row_mask:0xf bank_mask:0xf bound_ctrl:1
	v_pk_fma_f32 v[12:13], v[140:141], v[42:43], v[44:45]
	v_pk_mul_f32 v[42:43], v[148:149], v[8:9]
	v_mov_b32_dpp v27, v9 quad_perm:[2,3,0,1] row_mask:0xf bank_mask:0xf bound_ctrl:1
	v_pk_fma_f32 v[8:9], v[144:145], v[26:27], v[42:43]
	v_bfe_u32 v42, v17, 16, 1
	v_bfe_u32 v26, v9, 16, 1
	v_bfe_u32 v27, v8, 16, 1
	v_bfe_u32 v43, v16, 16, 1
	v_add3_u32 v16, v16, v43, s23
	v_add3_u32 v17, v17, v42, s23
	v_add3_u32 v8, v8, v27, s23
	v_add3_u32 v9, v9, v26, s23
	v_bfe_u32 v26, v20, 16, 1
	v_bfe_u32 v27, v21, 16, 1
	v_bfe_u32 v42, v12, 16, 1
	v_bfe_u32 v43, v13, 16, 1
	v_add3_u32 v13, v13, v43, s23
	v_add3_u32 v12, v12, v42, s23
	v_add3_u32 v21, v21, v27, s23
	v_add3_u32 v20, v20, v26, s23
	v_lshrrev_b32_e32 v20, 16, v20
	v_lshrrev_b32_e32 v21, 16, v21
	v_lshrrev_b32_e32 v12, 16, v12
	v_lshrrev_b32_e32 v13, 16, v13
	v_and_or_b32 v45, v9, s95, v13
	v_and_or_b32 v44, v8, s95, v12
	v_and_or_b32 v43, v17, s95, v21
	v_and_or_b32 v42, v16, s95, v20
	global_store_dwordx4 v[178:179], v[42:45], off nt
	v_lshlrev_b32_e32 v8, 16, v38
	v_and_b32_e32 v12, 0xffff0000, v38
	v_lshlrev_b32_e32 v44, 16, v30
	v_and_b32_e32 v30, 0xffff0000, v30
	v_mov_b32_e32 v16, v8
	v_mov_b32_e32 v17, v12
	v_mov_b32_e32 v46, v44
	v_mov_b32_e32 v47, v30
	v_lshlrev_b32_e32 v9, 16, v39
	v_and_b32_e32 v13, 0xffff0000, v39
	v_pk_mul_f32 v[16:17], v[16:17], v[16:17]
	v_lshlrev_b32_e32 v45, 16, v31
	v_and_b32_e32 v31, 0xffff0000, v31
	v_pk_mul_f32 v[46:47], v[46:47], v[46:47]
	v_mov_b32_e32 v20, v13
	v_mov_b32_e32 v21, v9
	v_mov_b32_e32 v48, v46
	v_mov_b32_e32 v49, v16
	v_mov_b32_e32 v16, v47
	v_mov_b32_e32 v46, v31
	v_mov_b32_e32 v47, v45
	v_pk_mul_f32 v[20:21], v[20:21], v[20:21]
	v_lshlrev_b32_e32 v26, 16, v40
	v_and_b32_e32 v38, 0xffff0000, v40
	v_pk_add_f32 v[16:17], v[48:49], v[16:17]
	v_pk_mul_f32 v[46:47], v[46:47], v[46:47]
	v_lshlrev_b32_e32 v48, 16, v32
	v_and_b32_e32 v32, 0xffff0000, v32
	v_lshlrev_b32_e32 v27, 16, v41
	v_and_b32_e32 v39, 0xffff0000, v41
	v_mov_b32_e32 v40, v38
	v_mov_b32_e32 v41, v26
	v_mov_b32_e32 v50, v32
	v_mov_b32_e32 v51, v48
	v_mov_b32_e32 v54, v47
	v_mov_b32_e32 v55, v21
	v_pk_mul_f32 v[40:41], v[40:41], v[40:41]
	v_lshlrev_b32_e32 v49, 16, v33
	v_and_b32_e32 v33, 0xffff0000, v33
	v_pk_mul_f32 v[50:51], v[50:51], v[50:51]
	v_pk_add_f32 v[16:17], v[54:55], v[16:17]
	v_mov_b32_e32 v47, v20
	v_mov_b32_e32 v42, v39
	v_mov_b32_e32 v43, v27
	v_mov_b32_e32 v52, v33
	v_mov_b32_e32 v53, v49
	v_pk_add_f32 v[16:17], v[46:47], v[16:17]
	v_mov_b32_e32 v20, v51
	v_mov_b32_e32 v21, v41
	v_pk_mul_f32 v[42:43], v[42:43], v[42:43]
; __device__ __forceinline__ unsigned pk2(float lo, float hi) { return f2bf(lo) | (f2bf(hi) << 16); }
; __device__ __forceinline__ float dpp_x1(float v) { return __builtin_bit_cast(float, __builtin_amdgcn_update_dpp(0, __builtin_bit_cast(int, v), 0xB1, 0xF, 0xF, true)); }
; __device__ __forceinline__ float dpp_x2(float v) { return __builtin_bit_cast(float, __builtin_amdgcn_update_dpp(0, __builtin_bit_cast(int, v), 0x4E, 0xF, 0xF, true)); }
; __device__ __forceinline__ float dpp_hm(float v) { return __builtin_bit_cast(float, __builtin_amdgcn_update_dpp(0, __builtin_bit_cast(int, v), 0x141, 0xF, 0xF, true)); }
; __device__ __forceinline__ void qk_vec(bf16_t* p, const u32x4 r, const float (&w)[8], const float (&cs)[8], const float (&sn)[8]) {
;     float x[8] = {bflo(r.x), bfhi(r.x), bflo(r.y), bfhi(r.y), bflo(r.z), bfhi(r.z), bflo(r.w), bfhi(r.w)};
;     float ss = 0.f;
; #pragma unroll
;     for (int e = 0; e < 8; ++e) ss += x[e] * x[e];
;     ss += dpp_x1(ss); ss += dpp_x2(ss); ss += dpp_hm(ss);
;     const float rstd = rsqrtf(ss * (1.f / 64.f) + NORM_EPS);
;     float o[8];
; #pragma unroll
;     for (int e = 0; e < 8; ++e) { const float y = x[e] * rstd * w[e]; o[e] = y * cs[e] + dpp_x2(y) * sn[e]; }
;     u32x4 q; q.x = pk2(o[0], o[1]); q.y = pk2(o[2], o[3]); q.z = pk2(o[4], o[5]); q.w = pk2(o[6], o[7]);
;     *(u32x4*)p = q;
; }
; __device__ __forceinline__ void prep_qk_rows4(KP Pk, Frame& F, int l, int row0) {
;     ...
; #pragma unroll
;     for (int r = 0; r < 4; ++r) { bf16_t* up = U + (size_t)(row0 + r) * NU + 8 * F.lane;
;         qk_vec(up + UC_SQ, raw[r][0], wsq, cs[r], sn[r]); qk_vec(up + UC_DQ, raw[r][1], wdq, cs[r], sn[r]); qk_vec(up + UC_DK, raw[r][2], wdk, cs[r], sn[r]); }
;     qk_vec(U + (size_t)rowk * NU + UC_SK + 8 * (F.lane & 15), rawk, wsk, csk, snk);
	v_pk_mul_f32 v[52:53], v[52:53], v[52:53]
	v_pk_add_f32 v[16:17], v[20:21], v[16:17]
	v_mov_b32_e32 v51, v40
	v_pk_add_f32 v[16:17], v[50:51], v[16:17]
	v_mov_b32_e32 v20, v53
	v_mov_b32_e32 v21, v43
	v_pk_add_f32 v[16:17], v[20:21], v[16:17]
	v_mov_b32_e32 v53, v42
	v_pk_add_f32 v[16:17], v[52:53], v[16:17]
	s_nop 1
	v_mov_b32_dpp v21, v17 quad_perm:[1,0,3,2] row_mask:0xf bank_mask:0xf bound_ctrl:1
	v_mov_b32_dpp v20, v16 quad_perm:[1,0,3,2] row_mask:0xf bank_mask:0xf bound_ctrl:1
	v_pk_add_f32 v[16:17], v[16:17], v[20:21]
	s_nop 1
	v_mov_b32_dpp v21, v17 quad_perm:[2,3,0,1] row_mask:0xf bank_mask:0xf bound_ctrl:1
	v_mov_b32_dpp v20, v16 quad_perm:[2,3,0,1] row_mask:0xf bank_mask:0xf bound_ctrl:1
	v_pk_add_f32 v[16:17], v[16:17], v[20:21]
	s_nop 1
	v_mov_b32_dpp v21, v17 row_half_mirror row_mask:0xf bank_mask:0xf bound_ctrl:1
	v_mov_b32_dpp v20, v16 row_half_mirror row_mask:0xf bank_mask:0xf bound_ctrl:1
	v_pk_add_f32 v[16:17], v[16:17], v[20:21]
	v_mov_b32_e32 v21, v24
	v_pk_fma_f32 v[16:17], v[16:17], s[8:9], v[92:93] op_sel_hi:[1,0,0]
	v_mov_b32_e32 v24, v23
	v_mul_f32_e32 v20, 0x4b800000, v17
	v_cmp_gt_f32_e32 vcc, s66, v17
	s_mov_b64 s[8:9], 0
	s_nop 0
	v_cndmask_b32_e32 v17, v17, v20, vcc
	v_rsq_f32_e32 v17, v17
	v_mov_b32_e32 v20, v22
	v_mul_f32_e32 v22, 0x45800000, v17
	v_cndmask_b32_e32 v22, v17, v22, vcc
	v_pk_mul_f32 v[8:9], v[22:23], v[8:9] op_sel_hi:[0,1]
	v_pk_mul_f32 v[8:9], v[90:91], v[8:9]
	v_pk_mul_f32 v[12:13], v[22:23], v[12:13] op_sel_hi:[0,1]
	v_pk_mul_f32 v[12:13], v[36:37], v[12:13]
	v_mov_b32_dpp v40, v8 quad_perm:[2,3,0,1] row_mask:0xf bank_mask:0xf bound_ctrl:1
	v_pk_mul_f32 v[10:11], v[10:11], v[8:9]
	v_mov_b32_dpp v41, v9 quad_perm:[2,3,0,1] row_mask:0xf bank_mask:0xf bound_ctrl:1
	v_mov_b32_dpp v36, v12 quad_perm:[2,3,0,1] row_mask:0xf bank_mask:0xf bound_ctrl:1
	v_pk_fma_f32 v[8:9], v[142:143], v[40:41], v[10:11]
	v_pk_mul_f32 v[10:11], v[150:151], v[12:13]
	v_mov_b32_dpp v37, v13 quad_perm:[2,3,0,1] row_mask:0xf bank_mask:0xf bound_ctrl:1
	v_pk_mul_f32 v[12:13], v[22:23], v[26:27] op_sel_hi:[0,1]
	v_pk_mul_f32 v[22:23], v[22:23], v[38:39] op_sel_hi:[0,1]
	v_pk_mul_f32 v[12:13], v[34:35], v[12:13]
	v_pk_mul_f32 v[22:23], v[28:29], v[22:23]
	v_pk_fma_f32 v[10:11], v[146:147], v[36:37], v[10:11]
	v_mov_b32_dpp v26, v12 quad_perm:[2,3,0,1] row_mask:0xf bank_mask:0xf bound_ctrl:1
	v_mov_b32_dpp v28, v22 quad_perm:[2,3,0,1] row_mask:0xf bank_mask:0xf bound_ctrl:1
	v_pk_mul_f32 v[6:7], v[6:7], v[12:13]
	v_mov_b32_dpp v27, v13 quad_perm:[2,3,0,1] row_mask:0xf bank_mask:0xf bound_ctrl:1
	v_pk_mul_f32 v[12:13], v[148:149], v[22:23]
	v_mov_b32_dpp v29, v23 quad_perm:[2,3,0,1] row_mask:0xf bank_mask:0xf bound_ctrl:1
	v_pk_fma_f32 v[6:7], v[140:141], v[26:27], v[6:7]
	v_pk_fma_f32 v[12:13], v[144:145], v[28:29], v[12:13]
	v_bfe_u32 v23, v11, 16, 1
	v_bfe_u32 v17, v13, 16, 1
	v_add3_u32 v11, v11, v23, s23
	v_bfe_u32 v23, v6, 16, 1
	v_bfe_u32 v22, v12, 16, 1
	v_add3_u32 v13, v13, v17, s23
	v_bfe_u32 v17, v8, 16, 1
	v_add3_u32 v6, v6, v23, s23
	v_add3_u32 v12, v12, v22, s23
	v_add3_u32 v8, v8, v17, s23
	v_lshrrev_b32_e32 v6, 16, v6
	v_lshrrev_b32_e32 v17, 16, v8
	v_and_or_b32 v8, v12, s95, v6
	v_mul_f32_e32 v6, 0x4b800000, v16
	v_cmp_gt_f32_e32 vcc, s66, v16
	v_bfe_u32 v26, v10, 16, 1
	v_add3_u32 v10, v10, v26, s23
	v_cndmask_b32_e32 v6, v16, v6, vcc
	v_bfe_u32 v22, v9, 16, 1
	v_bfe_u32 v26, v7, 16, 1
	v_rsq_f32_e32 v12, v6
	v_add3_u32 v7, v7, v26, s23
	v_add3_u32 v9, v9, v22, s23
	v_lshrrev_b32_e32 v22, 16, v9
	v_lshrrev_b32_e32 v7, 16, v7
	v_and_or_b32 v9, v13, s95, v7
	v_and_or_b32 v7, v11, s95, v22
	v_and_or_b32 v6, v10, s95, v17
	global_store_dwordx4 v[164:165], v[6:9], off nt
	s_nop 1
	v_mul_f32_e32 v6, 0x45800000, v12
	v_cndmask_b32_e32 v6, v12, v6, vcc
	v_pk_mul_f32 v[8:9], v[6:7], v[44:45] op_sel_hi:[0,1]
	v_pk_mul_f32 v[8:9], v[20:21], v[8:9]
	v_pk_mul_f32 v[12:13], v[6:7], v[30:31] op_sel_hi:[0,1]
	v_pk_mul_f32 v[12:13], v[24:25], v[12:13]
	v_mov_b32_dpp v10, v8 quad_perm:[2,3,0,1] row_mask:0xf bank_mask:0xf bound_ctrl:1
	v_pk_mul_f32 v[18:19], v[18:19], v[8:9]
	v_mov_b32_dpp v11, v9 quad_perm:[2,3,0,1] row_mask:0xf bank_mask:0xf bound_ctrl:1
	v_mov_b32_dpp v16, v12 quad_perm:[2,3,0,1] row_mask:0xf bank_mask:0xf bound_ctrl:1
	v_pk_fma_f32 v[8:9], v[154:155], v[10:11], v[18:19]
	v_pk_mul_f32 v[10:11], v[138:139], v[12:13]
	v_mov_b32_dpp v17, v13 quad_perm:[2,3,0,1] row_mask:0xf bank_mask:0xf bound_ctrl:1
	v_pk_fma_f32 v[10:11], v[156:157], v[16:17], v[10:11]
	v_pk_mul_f32 v[12:13], v[6:7], v[48:49] op_sel_hi:[0,1]
	v_mov_b32_e32 v16, v2
	v_mov_b32_e32 v17, v4
	v_pk_mul_f32 v[6:7], v[6:7], v[32:33] op_sel_hi:[0,1]
	v_mov_b32_e32 v4, v3
	v_pk_mul_f32 v[12:13], v[16:17], v[12:13]
	v_pk_mul_f32 v[4:5], v[4:5], v[6:7]
	v_pk_mul_f32 v[14:15], v[14:15], v[12:13]
	v_mov_b32_dpp v2, v12 quad_perm:[2,3,0,1] row_mask:0xf bank_mask:0xf bound_ctrl:1
	v_mov_b32_dpp v6, v4 quad_perm:[2,3,0,1] row_mask:0xf bank_mask:0xf bound_ctrl:1
	v_mov_b32_dpp v3, v13 quad_perm:[2,3,0,1] row_mask:0xf bank_mask:0xf bound_ctrl:1
	v_pk_mul_f32 v[12:13], v[158:159], v[4:5]
	v_mov_b32_dpp v7, v5 quad_perm:[2,3,0,1] row_mask:0xf bank_mask:0xf bound_ctrl:1
	v_pk_fma_f32 v[4:5], v[136:137], v[6:7], v[12:13]
	v_pk_fma_f32 v[2:3], v[152:153], v[2:3], v[14:15]
	v_bfe_u32 v6, v5, 16, 1
	v_bfe_u32 v7, v4, 16, 1
	v_bfe_u32 v12, v11, 16, 1
	v_bfe_u32 v13, v10, 16, 1
	v_add3_u32 v10, v10, v13, s23
	v_add3_u32 v11, v11, v12, s23
	v_add3_u32 v4, v4, v7, s23
	v_add3_u32 v5, v5, v6, s23
	v_bfe_u32 v6, v8, 16, 1
	v_bfe_u32 v7, v9, 16, 1
	v_bfe_u32 v12, v2, 16, 1
	v_bfe_u32 v13, v3, 16, 1
	v_add3_u32 v3, v3, v13, s23
	v_add3_u32 v2, v2, v12, s23
	v_add3_u32 v7, v9, v7, s23
	v_add3_u32 v6, v8, v6, s23
	v_lshrrev_b32_e32 v6, 16, v6
	v_lshrrev_b32_e32 v7, 16, v7
	v_lshrrev_b32_e32 v2, 16, v2
	v_lshrrev_b32_e32 v3, 16, v3
	v_and_or_b32 v5, v5, s95, v3
	v_and_or_b32 v4, v4, s95, v2
	v_and_or_b32 v3, v11, s95, v7
	v_and_or_b32 v2, v10, s95, v6
	global_store_dwordx4 v[160:161], v[2:5], off nt

; #define LAS __attribute__((address_space(3)))
; __device__ __forceinline__ int perm16(int k) { return (k & 3) + 4 * ((k >> 3) & 1) + 8 * ((k >> 2) & 1); }
; template <bool PERMK, int NCOLS, class SRC>
; __device__ __forceinline__ void tile_transpose(LAS unsigned char* wl, int lane, bf16_t* dst, size_t dst_stride, const SRC& src) {
;     ...
;     const LAS unsigned short* ts = (const LAS unsigned short*)wl;
;     const int cc = lane & 7;
;     for (int dv = lane >> 3; dv < ncols; dv += 8) {
;         unsigned short e[8];
; #pragma unroll
;         for (int i = 0; i < 8; ++i) { const int p = 8 * cc + i, srow = PERMK ? ((p & ~15) + perm16(p & 15)) : p; e[i] = ts[srow * 130 + dv]; }
;         u32x4 o; o.x = e[0] | ((unsigned)e[1] << 16); o.y = e[2] | ((unsigned)e[3] << 16); o.z = e[4] | ((unsigned)e[5] << 16); o.w = e[6] | ((unsigned)e[7] << 16);
;         *(u32x4*)(dst + (size_t)dv * dst_stride + 8 * cc) = o; }
.LBB0_391:
	ds_read_u16 v6, v4
	ds_read_u16 v10, v4 offset:260
	ds_read_u16 v7, v4 offset:520
	ds_read_u16 v11, v4 offset:780
	ds_read_u16 v8, v4 offset:2080
	ds_read_u16 v12, v4 offset:2340
	ds_read_u16 v9, v4 offset:2600
	ds_read_u16 v13, v4 offset:2860
	v_add_u32_e32 v5, 8, v5
	v_cmp_lt_i32_e32 vcc, 55, v5
	s_waitcnt lgkmcnt(2)
	v_perm_b32 v8, v12, v8, s3
	v_perm_b32 v7, v11, v7, s3
	s_waitcnt lgkmcnt(0)
	v_perm_b32 v9, v13, v9, s3
	v_perm_b32 v6, v10, v6, s3
	v_add_u32_e32 v4, 16, v4
	s_or_b64 s[8:9], vcc, s[8:9]
	global_store_dwordx4 v[2:3], v[6:9], off nt
	v_lshl_add_u64 v[2:3], v[2:3], 0, s[50:51]
	s_andn2_b64 exec, exec, s[8:9]
	s_cbranch_execnz .LBB0_391

; #define LAS __attribute__((address_space(3)))
; __device__ __forceinline__ int perm16(int k) { return (k & 3) + 4 * ((k >> 3) & 1) + 8 * ((k >> 2) & 1); }
; template <bool PERMK, int NCOLS, class SRC>
; __device__ __forceinline__ void tile_transpose(LAS unsigned char* wl, int lane, bf16_t* dst, size_t dst_stride, const SRC& src) {
;     ...
;     const LAS unsigned short* ts = (const LAS unsigned short*)wl;
;     const int cc = lane & 7;
;     for (int dv = lane >> 3; dv < ncols; dv += 8) {
;         unsigned short e[8];
; #pragma unroll
;         for (int i = 0; i < 8; ++i) { const int p = 8 * cc + i, srow = PERMK ? ((p & ~15) + perm16(p & 15)) : p; e[i] = ts[srow * 130 + dv]; }
;         u32x4 o; o.x = e[0] | ((unsigned)e[1] << 16); o.y = e[2] | ((unsigned)e[3] << 16); o.z = e[4] | ((unsigned)e[5] << 16); o.w = e[6] | ((unsigned)e[7] << 16);
;         *(u32x4*)(dst + (size_t)dv * dst_stride + 8 * cc) = o; }
.LBB0_399:
	ds_read_u16 v6, v4
	ds_read_u16 v10, v4 offset:260
	ds_read_u16 v7, v4 offset:520
	ds_read_u16 v11, v4 offset:780
	ds_read_u16 v8, v4 offset:2080
	ds_read_u16 v12, v4 offset:2340
	ds_read_u16 v9, v4 offset:2600
	ds_read_u16 v13, v4 offset:2860
	v_add_u32_e32 v5, 8, v5
	v_cmp_lt_i32_e32 vcc, s75, v5
	s_waitcnt lgkmcnt(2)
	v_perm_b32 v8, v12, v8, s3
	v_perm_b32 v7, v11, v7, s3
	s_waitcnt lgkmcnt(0)
	v_perm_b32 v9, v13, v9, s3
	v_perm_b32 v6, v10, v6, s3
	v_add_u32_e32 v4, 16, v4
	s_or_b64 s[8:9], vcc, s[8:9]
	global_store_dwordx4 v[2:3], v[6:9], off nt
	v_lshl_add_u64 v[2:3], v[2:3], 0, s[34:35]
	s_andn2_b64 exec, exec, s[8:9]
	s_cbranch_execnz .LBB0_399

; #define LAS __attribute__((address_space(3)))
; __device__ __forceinline__ int perm16(int k) { return (k & 3) + 4 * ((k >> 3) & 1) + 8 * ((k >> 2) & 1); }
; template <bool PERMK, int NCOLS, class SRC>
; __device__ __forceinline__ void tile_transpose(LAS unsigned char* wl, int lane, bf16_t* dst, size_t dst_stride, const SRC& src) {
;     ...
;     const LAS unsigned short* ts = (const LAS unsigned short*)wl;
;     const int cc = lane & 7;
;     for (int dv = lane >> 3; dv < ncols; dv += 8) {
;         unsigned short e[8];
; #pragma unroll
;         for (int i = 0; i < 8; ++i) { const int p = 8 * cc + i, srow = PERMK ? ((p & ~15) + perm16(p & 15)) : p; e[i] = ts[srow * 130 + dv]; }
;         u32x4 o; o.x = e[0] | ((unsigned)e[1] << 16); o.y = e[2] | ((unsigned)e[3] << 16); o.z = e[4] | ((unsigned)e[5] << 16); o.w = e[6] | ((unsigned)e[7] << 16);
;         *(u32x4*)(dst + (size_t)dv * dst_stride + 8 * cc) = o; }
.LBB0_423:
	ds_read_u16 v6, v4
	ds_read_u16 v10, v4 offset:260
	ds_read_u16 v7, v4 offset:520
	ds_read_u16 v11, v4 offset:780
	ds_read_u16 v8, v4 offset:1040
	ds_read_u16 v12, v4 offset:1300
	ds_read_u16 v9, v4 offset:1560
	ds_read_u16 v13, v4 offset:1820
	v_add_u32_e32 v5, 8, v5
	v_cmp_lt_i32_e32 vcc, s75, v5
	s_waitcnt lgkmcnt(2)
	v_perm_b32 v8, v12, v8, s3
	v_perm_b32 v7, v11, v7, s3
	s_waitcnt lgkmcnt(0)
	v_perm_b32 v9, v13, v9, s3
	v_perm_b32 v6, v10, v6, s3
	v_add_u32_e32 v4, 16, v4
	s_or_b64 s[8:9], vcc, s[8:9]
	global_store_dwordx4 v[2:3], v[6:9], off nt
	v_lshl_add_u64 v[2:3], v[2:3], 0, s[50:51]
	s_andn2_b64 exec, exec, s[8:9]
	s_cbranch_execnz .LBB0_423
	s_branch .LBB0_364
